# mix1 light workgroups: published local states stored write-through (sc1) + vmcnt(0) drain, the 256 per-workgroup buffer_wbl2 in front of the published counter removed
# speedup vs baseline: 1.0060x; 1.0060x over previous
;     template <class T> __device__ __forceinline__ T* w(size_t off) const { return (T*)(p->ws + off); }
;     ...
;     if (DEEP == 1) {
;         gloadA(0, ra0); gloadB(0, rb0); gloadA(1, ra1);
;         for (int kt = 0; kt < nk; kt += 2) {
;             __syncthreads();
;             lstore(ra0, rb0);
;             __syncthreads();
;             gloadB(kt + 1, rb0);
; __device__ __forceinline__ void s5_gemm_s(const Ctx& c, int layer, int tile, unsigned char* lds) {
;     const int nt = tile & 1, mt = (tile >> 1) % 5, g = tile / 10;
;     const bf16* UH = c.w<bf16>(WS_UH) + (size_t)g * NCH5 * 768;
;     f32x4 acc[4][4];
;     const int bc = nt * 128 + (c.tid & 15) * 8;
;     gemm_tile<false, 1>(c.tid, lds, UH, [&](int r) __attribute__((always_inline)) { int row = mt * 128 + r; row = row < NCH5 ? row : NCH5 - 1; return (unsigned)(row * 768); },
;                      c.w<bf16>(WS_WS) + (size_t)(layer * 16 + g) * 512 * 256, (unsigned)bc, 256, true, 512, acc);
.LBB0_354:
	s_mov_b64 s[6:7], -1
	v_bfe_u32 v4, v147, 4, 2
	s_cmpk_gt_i32 s63, 0x21f
	v_and_b32_e32 v72, 15, v147
	v_lshlrev_b32_e32 v2, 4, v4
	v_lshlrev_b32_e32 v73, 3, v4
	s_cbranch_scc0 .LBB0_364
	s_add_i32 s6, s63, 0xfffffde0
	s_lshr_b32 s7, s6, 1
	s_mul_i32 s15, s7, 0xcd
	s_bfe_u32 s15, s15, 0x6000a
	s_load_dwordx2 s[42:43], s[0:1], 0x130
	s_mul_i32 s15, s15, 5
	s_sub_i32 s7, s7, s15
	s_mulk_i32 s6, 0xcd
	s_and_b32 s15, s7, 0xff
	s_bfe_u32 s7, s6, 0x5000b
	s_mul_i32 s6, s7, 0xcc000
	s_waitcnt lgkmcnt(0)
	s_add_u32 s6, s42, s6
	s_addc_u32 s16, s43, 0
	s_add_u32 s44, s6, 0x126dc000
	s_addc_u32 s45, s16, 0
	s_add_i32 s16, s58, s7
	s_ashr_i32 s17, s16, 31
	s_and_b32 s6, s59, 0x80
	s_lshl_b64 s[16:17], s[16:17], 18
	s_add_u32 s16, s42, s16
	s_addc_u32 s17, s43, s17
	s_add_u32 s28, s16, 0x11edc000
	s_addc_u32 s29, s17, 0
	v_ashrrev_i32_e32 v4, 3, v147
	s_lshl_b32 s15, s15, 7
	v_add_u32_e32 v5, s15, v4
	v_lshlrev_b32_e32 v34, 3, v147
	v_min_i32_e32 v4, 0x21f, v5
	s_movk_i32 s16, 0x300
	v_and_b32_e32 v7, 56, v34
	v_mul_lo_u32 v4, v4, s16
	v_or_b32_e32 v38, v4, v7
	v_min_i32_e32 v4, 0x1ff, v5
	v_mul_lo_u32 v4, v4, s16
	v_min_i32_e32 v6, 0x1df, v5
	v_min_i32_e32 v5, 0x1bf, v5
	v_or_b32_e32 v50, v4, v7
	v_mul_lo_u32 v5, v5, s16
	v_add_u32_e32 v4, 0x6000, v50
	v_or_b32_e32 v49, v5, v7
	v_ashrrev_i32_e32 v35, 4, v147
	v_mov_b32_e32 v5, v3
	v_and_b32_e32 v10, 0x78, v34
	v_mul_lo_u32 v6, v6, s16
	v_lshl_add_u64 v[40:41], v[4:5], 1, s[44:45]
	v_lshlrev_b32_e32 v4, 8, v35
	v_or_b32_e32 v48, v6, v7
	v_or3_b32 v36, v10, s6, v4
	v_mov_b32_e32 v37, v3
	v_add_u32_e32 v6, 0xc000, v48
	v_mov_b32_e32 v7, v3
	v_lshl_add_u64 v[4:5], v[36:37], 1, s[28:29]
	v_add_u32_e32 v8, 0x12000, v49
	v_mov_b32_e32 v39, v3
	v_lshl_add_u64 v[42:43], v[6:7], 1, s[44:45]
	v_mov_b32_e32 v9, v3
	v_add_co_u32_e32 v6, vcc, s65, v4
	v_lshl_add_u64 v[32:33], v[38:39], 1, s[44:45]
	v_lshl_add_u64 v[44:45], v[8:9], 1, s[44:45]
	v_addc_co_u32_e32 v7, vcc, 0, v5, vcc
	global_load_dwordx4 v[16:19], v[32:33], off
	global_load_dwordx4 v[20:23], v[40:41], off
	global_load_dwordx4 v[28:31], v[42:43], off
	global_load_dwordx4 v[52:55], v[44:45], off
	global_load_dwordx4 v[56:59], v[4:5], off
	global_load_dwordx4 v[60:63], v[6:7], off
	v_add_co_u32_e32 v6, vcc, s69, v4
	s_movk_i32 s16, 0x120
	s_nop 0
	v_addc_co_u32_e32 v7, vcc, 0, v5, vcc
	v_add_co_u32_e32 v4, vcc, s90, v4
	v_bfe_i32 v46, v147, 2, 1
	s_nop 0
	v_addc_co_u32_e32 v5, vcc, 0, v5, vcc
	global_load_dwordx4 v[64:67], v[6:7], off
	global_load_dwordx4 v[68:71], v[4:5], off
	v_bfe_u32 v5, v147, 4, 1
	v_bfe_u32 v4, v147, 2, 2
	v_lshlrev_b32_e32 v6, 2, v5
	v_or3_b32 v4, v73, v4, v6
	v_lshlrev_b32_e32 v6, 1, v147
	v_and_b32_e32 v6, 0x80, v6
	v_mad_u32_u24 v4, v4, s16, v6
	v_and_or_b32 v37, v34, 24, v4
	v_cmp_eq_u32_e32 vcc, 0, v5
	v_and_b32_e32 v74, 1, v147
	v_and_b32_e32 v46, 0x2040, v46
	v_and_b32_e32 v34, 0xffffffc0, v34
	v_cndmask_b32_e32 v39, v236, v237, vcc
	v_add_u32_e32 v34, v46, v34
	v_lshlrev_b32_e32 v46, 4, v147
	v_cmp_eq_u32_e32 vcc, 0, v74
	v_and_or_b32 v47, v46, 48, v34
	global_load_dwordx4 v[24:27], v[32:33], off offset:128
	global_load_dwordx4 v[12:15], v[40:41], off offset:128
	global_load_dwordx4 v[8:11], v[42:43], off offset:128
	global_load_dwordx4 v[4:7], v[44:45], off offset:128
	s_barrier
	v_ashrrev_i32_e32 v51, 1, v147
	v_mul_lo_u32 v34, v35, s16
	v_lshl_add_u32 v46, v72, 4, v34
	v_add_u32_e32 v39, v37, v39
	v_add_u32_e32 v34, 0x4000, v36
	v_mov_b32_e32 v35, v3
	v_lshl_add_u64 v[34:35], v[34:35], 1, s[28:29]
	s_mul_i32 s7, s7, 0x88000
	s_add_u32 s7, s42, s7
	s_addc_u32 s16, s43, 0
	s_waitcnt vmcnt(11)
	v_cndmask_b32_e32 v77, v17, v19, vcc
	v_cndmask_b32_e32 v76, v16, v18, vcc
	v_cndmask_b32_e32 v75, v19, v17, vcc
	v_cndmask_b32_e32 v74, v18, v16, vcc
	s_waitcnt vmcnt(10)
	v_cndmask_b32_e32 v19, v21, v23, vcc
	v_cndmask_b32_e32 v18, v20, v22, vcc
	v_cndmask_b32_e32 v17, v23, v21, vcc
	v_cndmask_b32_e32 v16, v22, v20, vcc
	ds_write_b128 v47, v[16:19] offset:2048
	s_waitcnt vmcnt(9)
	v_cndmask_b32_e32 v19, v29, v31, vcc
	v_cndmask_b32_e32 v18, v28, v30, vcc
	v_cndmask_b32_e32 v17, v31, v29, vcc
	v_cndmask_b32_e32 v16, v30, v28, vcc
	ds_write_b128 v47, v[16:19] offset:4096
	s_waitcnt vmcnt(8)
	v_cndmask_b32_e32 v19, v53, v55, vcc
	v_cndmask_b32_e32 v18, v52, v54, vcc
	v_cndmask_b32_e32 v17, v55, v53, vcc
	v_cndmask_b32_e32 v16, v54, v52, vcc
	ds_write_b128 v47, v[74:77]
	ds_write_b128 v47, v[16:19] offset:6144
	s_waitcnt vmcnt(7)
	ds_write_b128 v46, v[56:59] offset:16512
	s_waitcnt vmcnt(6)
	ds_write_b128 v46, v[60:63] offset:21120
	s_waitcnt vmcnt(5)
	ds_write_b128 v46, v[64:67] offset:25728
	s_waitcnt vmcnt(4)
	ds_write_b128 v46, v[68:71] offset:30336
	v_and_b32_e32 v68, 0xffffffc0, v51
	v_or_b32_e32 v20, v68, v72
	v_lshl_or_b32 v69, v20, 6, v2
	s_waitcnt lgkmcnt(0)
	s_barrier
; #define LAS __attribute__((address_space(3)))
; __device__ __forceinline__ s16x4 lds_tr(lds_cptr p) { return __builtin_bit_cast(s16x4, __builtin_amdgcn_ds_read_tr16_b64_v4i16((LAS s16x4*)p)); }
;     ...
;     auto compute = [&]() __attribute__((always_inline)) {
; #pragma unroll
;         for (int kh = 0; kh < 2; ++kh) {
;             bf16x8 af[4], bfr[4];
; #pragma unroll
;             for (int m = 0; m < 4; ++m) af[m] = *(const LAS bf16x8*)(la + kh * GA_KH + m * 1024);
; #pragma unroll
;             for (int n = 0; n < 4; ++n) {
;                 const s16x4 r0 = lds_tr(lb + kh * 32 * GB_ST + n * 32), r1 = lds_tr(lb + kh * 32 * GB_ST + n * 32 + bsw);
;                 bfr[n] = (bf16x8){r0[0], r0[1], r0[2], r0[3], r1[0], r1[1], r1[2], r1[3]};
;             }
; #pragma unroll
;             for (int m = 0; m < 4; ++m)
; #pragma unroll
;                 for (int n = 0; n < 4; ++n) acc[m][n] = __builtin_amdgcn_mfma_f32_16x16x32_bf16(bfr[n], af[m], acc[m][n], 0, 0, 0);
;         }
;     };
;     ...
;             gloadB(kt + 1, rb0);
;             if (kt + 2 < nk) gloadA(kt + 2, ra0);
;             compute();
;             __syncthreads();
;             lstore(ra1, rb0);
;             __syncthreads();
;             if (kt + 2 < nk) gloadB(kt + 2, rb0);
;             if (kt + 3 < nk) gloadA(kt + 3, ra1);
;             compute();
	ds_read_b64_tr_b16 v[16:17], v37 offset:16512
	ds_read_b64_tr_b16 v[18:19], v39 offset:16512
	ds_read_b128 v[20:23], v69
	ds_read_b64_tr_b16 v[30:31], v39 offset:16544
	ds_read_b64_tr_b16 v[28:29], v37 offset:16544
	ds_read_b64_tr_b16 v[56:57], v37 offset:16576
	ds_read_b64_tr_b16 v[58:59], v39 offset:16576
	ds_read_b64_tr_b16 v[64:65], v37 offset:16608
	ds_read_b64_tr_b16 v[66:67], v39 offset:16608
	ds_read_b128 v[78:81], v69 offset:1024
	ds_read_b128 v[94:97], v69 offset:2048
	ds_read_b128 v[110:113], v69 offset:3072
	s_waitcnt lgkmcnt(9)
	v_mfma_f32_16x16x32_bf16 v[52:55], v[16:19], v[20:23], 0
	ds_read_b64_tr_b16 v[114:115], v37 offset:25728
	ds_read_b64_tr_b16 v[116:117], v39 offset:25728
	v_add_co_u32_e64 v70, s[46:47], s65, v34
	s_waitcnt lgkmcnt(9)
	v_mfma_f32_16x16x32_bf16 v[60:63], v[28:31], v[20:23], 0
	v_addc_co_u32_e64 v71, s[46:47], 0, v35, s[46:47]
	s_waitcnt vmcnt(3)
	v_cndmask_b32_e32 v169, v25, v27, vcc
	s_waitcnt lgkmcnt(7)
	v_mfma_f32_16x16x32_bf16 v[74:77], v[56:59], v[20:23], 0
	v_cndmask_b32_e32 v168, v24, v26, vcc
	v_cndmask_b32_e32 v167, v27, v25, vcc
	v_cndmask_b32_e32 v166, v26, v24, vcc
	s_waitcnt lgkmcnt(5)
	v_mfma_f32_16x16x32_bf16 v[20:23], v[64:67], v[20:23], 0
	s_waitcnt vmcnt(2)
	v_cndmask_b32_e32 v27, v13, v15, vcc
	v_cndmask_b32_e32 v26, v12, v14, vcc
	v_cndmask_b32_e32 v25, v15, v13, vcc
	s_waitcnt lgkmcnt(4)
	v_mfma_f32_16x16x32_bf16 v[82:85], v[16:19], v[78:81], 0
	v_cndmask_b32_e32 v24, v14, v12, vcc
	s_waitcnt vmcnt(1)
	v_cndmask_b32_e32 v13, v9, v11, vcc
	v_cndmask_b32_e32 v12, v8, v10, vcc
	v_mfma_f32_16x16x32_bf16 v[86:89], v[28:31], v[78:81], 0
	v_cndmask_b32_e32 v11, v11, v9, vcc
	v_cndmask_b32_e32 v10, v10, v8, vcc
	s_waitcnt vmcnt(0)
	v_cndmask_b32_e32 v9, v5, v7, vcc
	v_mfma_f32_16x16x32_bf16 v[90:93], v[56:59], v[78:81], 0
	v_cndmask_b32_e32 v8, v4, v6, vcc
	v_cndmask_b32_e32 v7, v7, v5, vcc
	v_cndmask_b32_e32 v6, v6, v4, vcc
	v_mfma_f32_16x16x32_bf16 v[78:81], v[64:67], v[78:81], 0
	v_add_u32_e32 v68, s15, v68
	s_waitcnt lgkmcnt(3)
	v_mfma_f32_16x16x32_bf16 v[98:101], v[16:19], v[94:97], 0
	v_mfma_f32_16x16x32_bf16 v[102:105], v[28:31], v[94:97], 0
	v_mfma_f32_16x16x32_bf16 v[106:109], v[56:59], v[94:97], 0
	v_mfma_f32_16x16x32_bf16 v[94:97], v[64:67], v[94:97], 0
	s_waitcnt lgkmcnt(2)
	v_mfma_f32_16x16x32_bf16 v[16:19], v[16:19], v[110:113], 0
	v_mfma_f32_16x16x32_bf16 v[28:31], v[28:31], v[110:113], 0
	v_mfma_f32_16x16x32_bf16 v[56:59], v[56:59], v[110:113], 0
	v_mfma_f32_16x16x32_bf16 v[64:67], v[64:67], v[110:113], 0
	ds_read_b128 v[110:113], v69 offset:8256
	ds_read_b64_tr_b16 v[120:121], v39 offset:25760
	ds_read_b64_tr_b16 v[118:119], v37 offset:25760
	ds_read_b64_tr_b16 v[122:123], v37 offset:25792
	ds_read_b64_tr_b16 v[124:125], v39 offset:25792
	ds_read_b64_tr_b16 v[126:127], v37 offset:25824
	ds_read_b64_tr_b16 v[128:129], v39 offset:25824
	ds_read_b128 v[130:133], v69 offset:11328
	s_waitcnt lgkmcnt(7)
	v_mfma_f32_16x16x32_bf16 v[52:55], v[114:117], v[110:113], v[52:55]
	s_waitcnt lgkmcnt(5)
	v_mfma_f32_16x16x32_bf16 v[60:63], v[118:121], v[110:113], v[60:63]
	s_waitcnt lgkmcnt(3)
	v_mfma_f32_16x16x32_bf16 v[74:77], v[122:125], v[110:113], v[74:77]
	s_waitcnt lgkmcnt(1)
	v_mfma_f32_16x16x32_bf16 v[110:113], v[126:129], v[110:113], v[20:23]
	s_nop 2
	ds_read_b128 v[20:23], v69 offset:9280
	s_waitcnt lgkmcnt(0)
	v_mfma_f32_16x16x32_bf16 v[82:85], v[114:117], v[20:23], v[82:85]
	v_mfma_f32_16x16x32_bf16 v[86:89], v[118:121], v[20:23], v[86:89]
	v_mfma_f32_16x16x32_bf16 v[90:93], v[122:125], v[20:23], v[90:93]
	v_mfma_f32_16x16x32_bf16 v[78:81], v[126:129], v[20:23], v[78:81]
	ds_read_b128 v[20:23], v69 offset:10304
	global_load_dwordx4 v[134:137], v[34:35], off
	global_load_dwordx4 v[138:141], v[70:71], off
	s_waitcnt lgkmcnt(0)
	v_mfma_f32_16x16x32_bf16 v[98:101], v[114:117], v[20:23], v[98:101]
	v_mfma_f32_16x16x32_bf16 v[102:105], v[118:121], v[20:23], v[102:105]
	v_mfma_f32_16x16x32_bf16 v[106:109], v[122:125], v[20:23], v[106:109]
	v_mfma_f32_16x16x32_bf16 v[94:97], v[126:129], v[20:23], v[94:97]
	v_add_co_u32_e64 v20, s[46:47], s69, v34
	s_nop 1
	v_addc_co_u32_e64 v21, s[46:47], 0, v35, s[46:47]
	v_mfma_f32_16x16x32_bf16 v[114:117], v[114:117], v[130:133], v[16:19]
	s_nop 2
	v_add_co_u32_e64 v16, s[46:47], s90, v34
	v_mfma_f32_16x16x32_bf16 v[118:121], v[118:121], v[130:133], v[28:31]
	s_nop 0
	v_addc_co_u32_e64 v17, s[46:47], 0, v35, s[46:47]
	global_load_dwordx4 v[158:161], v[20:21], off
	global_load_dwordx4 v[162:165], v[16:17], off
	v_mfma_f32_16x16x32_bf16 v[56:59], v[122:125], v[130:133], v[56:59]
	global_load_dwordx4 v[122:125], v[32:33], off offset:256
	global_load_dwordx4 v[28:31], v[40:41], off offset:256
	global_load_dwordx4 v[20:23], v[42:43], off offset:256
	global_load_dwordx4 v[16:19], v[44:45], off offset:256
	s_barrier
	ds_write_b128 v47, v[166:169]
	ds_write_b128 v47, v[24:27] offset:2048
	ds_write_b128 v47, v[10:13] offset:4096
	ds_write_b128 v47, v[6:9] offset:6144
	s_waitcnt vmcnt(7)
	ds_write_b128 v46, v[134:137] offset:16512
	s_waitcnt vmcnt(6)
	ds_write_b128 v46, v[138:141] offset:21120
	s_waitcnt vmcnt(5)
	ds_write_b128 v46, v[158:161] offset:25728
	s_waitcnt vmcnt(4)
	ds_write_b128 v46, v[162:165] offset:30336
	s_waitcnt lgkmcnt(0)
	s_barrier
; #define LAS __attribute__((address_space(3)))
; __device__ __forceinline__ s16x4 lds_tr(lds_cptr p) { return __builtin_bit_cast(s16x4, __builtin_amdgcn_ds_read_tr16_b64_v4i16((LAS s16x4*)p)); }
;     ...
;     auto compute = [&]() __attribute__((always_inline)) {
; #pragma unroll
;         for (int kh = 0; kh < 2; ++kh) {
;             bf16x8 af[4], bfr[4];
; #pragma unroll
;             for (int m = 0; m < 4; ++m) af[m] = *(const LAS bf16x8*)(la + kh * GA_KH + m * 1024);
; #pragma unroll
;             for (int n = 0; n < 4; ++n) {
;                 const s16x4 r0 = lds_tr(lb + kh * 32 * GB_ST + n * 32), r1 = lds_tr(lb + kh * 32 * GB_ST + n * 32 + bsw);
;                 bfr[n] = (bf16x8){r0[0], r0[1], r0[2], r0[3], r1[0], r1[1], r1[2], r1[3]};
;             }
; #pragma unroll
;             for (int m = 0; m < 4; ++m)
; #pragma unroll
;                 for (int n = 0; n < 4; ++n) acc[m][n] = __builtin_amdgcn_mfma_f32_16x16x32_bf16(bfr[n], af[m], acc[m][n], 0, 0, 0);
;         }
;     };
;     ...
;             __syncthreads();
;             lstore(ra1, rb0);
;             __syncthreads();
;             if (kt + 2 < nk) gloadB(kt + 2, rb0);
;             if (kt + 3 < nk) gloadA(kt + 3, ra1);
;             compute();
	ds_read_b64_tr_b16 v[4:5], v37 offset:16512
	ds_read_b64_tr_b16 v[6:7], v39 offset:16512
	v_mfma_f32_16x16x32_bf16 v[8:11], v[126:129], v[130:133], v[64:67]
	ds_read_b128 v[12:15], v69
	ds_read_b64_tr_b16 v[26:27], v39 offset:16544
	ds_read_b64_tr_b16 v[24:25], v37 offset:16544
	ds_read_b64_tr_b16 v[64:65], v37 offset:16576
	ds_read_b64_tr_b16 v[66:67], v39 offset:16576
	ds_read_b64_tr_b16 v[126:127], v37 offset:16608
	ds_read_b64_tr_b16 v[128:129], v39 offset:16608
	s_waitcnt lgkmcnt(6)
	v_mfma_f32_16x16x32_bf16 v[52:55], v[4:7], v[12:15], v[52:55]
	v_add_u32_e32 v34, 0x8000, v36
	v_mov_b32_e32 v35, v3
	v_lshl_add_u64 v[34:35], v[34:35], 1, s[28:29]
	s_waitcnt lgkmcnt(4)
	v_mfma_f32_16x16x32_bf16 v[60:63], v[24:27], v[12:15], v[60:63]
	v_add_co_u32_e64 v70, s[46:47], s65, v34
	s_waitcnt lgkmcnt(2)
	v_mfma_f32_16x16x32_bf16 v[74:77], v[64:67], v[12:15], v[74:77]
	v_addc_co_u32_e64 v71, s[46:47], 0, v35, s[46:47]
	s_waitcnt lgkmcnt(0)
	v_mfma_f32_16x16x32_bf16 v[12:15], v[126:129], v[12:15], v[110:113]
	s_nop 2
	ds_read_b128 v[110:113], v69 offset:1024
	s_waitcnt lgkmcnt(0)
	v_mfma_f32_16x16x32_bf16 v[82:85], v[4:7], v[110:113], v[82:85]
	v_mfma_f32_16x16x32_bf16 v[86:89], v[24:27], v[110:113], v[86:89]
	v_mfma_f32_16x16x32_bf16 v[90:93], v[64:67], v[110:113], v[90:93]
	v_mfma_f32_16x16x32_bf16 v[78:81], v[126:129], v[110:113], v[78:81]
	ds_read_b128 v[110:113], v69 offset:2048
	s_waitcnt lgkmcnt(0)
	v_mfma_f32_16x16x32_bf16 v[98:101], v[4:7], v[110:113], v[98:101]
	v_mfma_f32_16x16x32_bf16 v[102:105], v[24:27], v[110:113], v[102:105]
	v_mfma_f32_16x16x32_bf16 v[106:109], v[64:67], v[110:113], v[106:109]
	v_mfma_f32_16x16x32_bf16 v[94:97], v[126:129], v[110:113], v[94:97]
	ds_read_b128 v[110:113], v69 offset:3072
	s_waitcnt lgkmcnt(0)
	v_mfma_f32_16x16x32_bf16 v[4:7], v[4:7], v[110:113], v[114:117]
	v_mfma_f32_16x16x32_bf16 v[24:27], v[24:27], v[110:113], v[118:121]
	v_mfma_f32_16x16x32_bf16 v[56:59], v[64:67], v[110:113], v[56:59]
	ds_read_b64_tr_b16 v[64:65], v37 offset:25728
	ds_read_b64_tr_b16 v[66:67], v39 offset:25728
	v_mfma_f32_16x16x32_bf16 v[8:11], v[126:129], v[110:113], v[8:11]
	ds_read_b128 v[110:113], v69 offset:8256
	ds_read_b64_tr_b16 v[116:117], v39 offset:25760
	ds_read_b64_tr_b16 v[114:115], v37 offset:25760
	ds_read_b64_tr_b16 v[118:119], v37 offset:25792
	ds_read_b64_tr_b16 v[120:121], v39 offset:25792
	ds_read_b64_tr_b16 v[126:127], v37 offset:25824
	ds_read_b64_tr_b16 v[128:129], v39 offset:25824
	ds_read_b128 v[130:133], v69 offset:11328
	s_waitcnt lgkmcnt(7)
	v_mfma_f32_16x16x32_bf16 v[52:55], v[64:67], v[110:113], v[52:55]
	s_waitcnt lgkmcnt(5)
	v_mfma_f32_16x16x32_bf16 v[60:63], v[114:117], v[110:113], v[60:63]
	s_waitcnt lgkmcnt(3)
	v_mfma_f32_16x16x32_bf16 v[74:77], v[118:121], v[110:113], v[74:77]
	s_waitcnt lgkmcnt(1)
	v_mfma_f32_16x16x32_bf16 v[110:113], v[126:129], v[110:113], v[12:15]
	s_nop 2
	ds_read_b128 v[12:15], v69 offset:9280
	s_waitcnt lgkmcnt(0)
	v_mfma_f32_16x16x32_bf16 v[82:85], v[64:67], v[12:15], v[82:85]
	v_mfma_f32_16x16x32_bf16 v[86:89], v[114:117], v[12:15], v[86:89]
	v_mfma_f32_16x16x32_bf16 v[90:93], v[118:121], v[12:15], v[90:93]
	v_mfma_f32_16x16x32_bf16 v[78:81], v[126:129], v[12:15], v[78:81]
	ds_read_b128 v[12:15], v69 offset:10304
	global_load_dwordx4 v[134:137], v[34:35], off
	global_load_dwordx4 v[138:141], v[70:71], off
	s_waitcnt lgkmcnt(0)
	v_mfma_f32_16x16x32_bf16 v[98:101], v[64:67], v[12:15], v[98:101]
	v_mfma_f32_16x16x32_bf16 v[102:105], v[114:117], v[12:15], v[102:105]
	v_mfma_f32_16x16x32_bf16 v[106:109], v[118:121], v[12:15], v[106:109]
	v_mfma_f32_16x16x32_bf16 v[94:97], v[126:129], v[12:15], v[94:97]
	v_add_co_u32_e64 v12, s[46:47], s69, v34
	s_nop 1
	v_addc_co_u32_e64 v13, s[46:47], 0, v35, s[46:47]
	v_mfma_f32_16x16x32_bf16 v[64:67], v[64:67], v[130:133], v[4:7]
	s_nop 2
	v_add_co_u32_e64 v4, s[46:47], s90, v34
	v_mfma_f32_16x16x32_bf16 v[114:117], v[114:117], v[130:133], v[24:27]
	s_nop 0
	v_addc_co_u32_e64 v5, s[46:47], 0, v35, s[46:47]
	global_load_dwordx4 v[158:161], v[12:13], off
	global_load_dwordx4 v[162:165], v[4:5], off
	s_nop 0
	global_load_dwordx4 v[32:35], v[32:33], off offset:384
	s_nop 0
	global_load_dwordx4 v[24:27], v[40:41], off offset:384
	global_load_dwordx4 v[12:15], v[42:43], off offset:384
	global_load_dwordx4 v[4:7], v[44:45], off offset:384
	s_waitcnt vmcnt(11)
	v_cndmask_b32_e32 v43, v123, v125, vcc
	v_cndmask_b32_e32 v42, v122, v124, vcc
	v_cndmask_b32_e32 v41, v125, v123, vcc
	v_cndmask_b32_e32 v40, v124, v122, vcc
	s_barrier
	ds_write_b128 v47, v[40:43]
	s_waitcnt vmcnt(10)
	v_cndmask_b32_e32 v43, v29, v31, vcc
	v_cndmask_b32_e32 v42, v28, v30, vcc
	v_cndmask_b32_e32 v41, v31, v29, vcc
	v_cndmask_b32_e32 v40, v30, v28, vcc
	s_waitcnt vmcnt(9)
	v_cndmask_b32_e32 v31, v21, v23, vcc
	v_cndmask_b32_e32 v30, v20, v22, vcc
	v_cndmask_b32_e32 v29, v23, v21, vcc
	v_cndmask_b32_e32 v28, v22, v20, vcc
	s_waitcnt vmcnt(8)
	v_cndmask_b32_e32 v21, v17, v19, vcc
	v_cndmask_b32_e32 v20, v16, v18, vcc
	v_cndmask_b32_e32 v19, v19, v17, vcc
	v_cndmask_b32_e32 v18, v18, v16, vcc
	ds_write_b128 v47, v[40:43] offset:2048
	ds_write_b128 v47, v[28:31] offset:4096
	ds_write_b128 v47, v[18:21] offset:6144
	s_waitcnt vmcnt(7)
	ds_write_b128 v46, v[134:137] offset:16512
	s_waitcnt vmcnt(6)
	ds_write_b128 v46, v[138:141] offset:21120
	s_waitcnt vmcnt(5)
	ds_write_b128 v46, v[158:161] offset:25728
	s_waitcnt vmcnt(4)
	ds_write_b128 v46, v[162:165] offset:30336
	s_waitcnt lgkmcnt(0)
	s_barrier
; #define LAS __attribute__((address_space(3)))
; __device__ __forceinline__ s16x4 lds_tr(lds_cptr p) { return __builtin_bit_cast(s16x4, __builtin_amdgcn_ds_read_tr16_b64_v4i16((LAS s16x4*)p)); }
;     ...
;     auto compute = [&]() __attribute__((always_inline)) {
; #pragma unroll
;         for (int kh = 0; kh < 2; ++kh) {
;             bf16x8 af[4], bfr[4];
; #pragma unroll
;             for (int m = 0; m < 4; ++m) af[m] = *(const LAS bf16x8*)(la + kh * GA_KH + m * 1024);
; #pragma unroll
;             for (int n = 0; n < 4; ++n) {
;                 const s16x4 r0 = lds_tr(lb + kh * 32 * GB_ST + n * 32), r1 = lds_tr(lb + kh * 32 * GB_ST + n * 32 + bsw);
;                 bfr[n] = (bf16x8){r0[0], r0[1], r0[2], r0[3], r1[0], r1[1], r1[2], r1[3]};
;             }
; #pragma unroll
;             for (int m = 0; m < 4; ++m)
; #pragma unroll
;                 for (int n = 0; n < 4; ++n) acc[m][n] = __builtin_amdgcn_mfma_f32_16x16x32_bf16(bfr[n], af[m], acc[m][n], 0, 0, 0);
;         }
;     };
;     ...
;             gloadB(kt + 1, rb0);
;             if (kt + 2 < nk) gloadA(kt + 2, ra0);
;             compute();
;             __syncthreads();
;             lstore(ra1, rb0);
;             __syncthreads();
;             if (kt + 2 < nk) gloadB(kt + 2, rb0);
;             if (kt + 3 < nk) gloadA(kt + 3, ra1);
;             compute();
	ds_read_b64_tr_b16 v[16:17], v37 offset:16512
	ds_read_b64_tr_b16 v[18:19], v39 offset:16512
	ds_read_b128 v[20:23], v69
	ds_read_b64_tr_b16 v[30:31], v39 offset:16544
	v_mfma_f32_16x16x32_bf16 v[56:59], v[118:121], v[130:133], v[56:59]
	s_waitcnt lgkmcnt(1)
	v_mfma_f32_16x16x32_bf16 v[40:43], v[16:19], v[20:23], v[52:55]
	ds_read_b64_tr_b16 v[28:29], v37 offset:16544
	s_nop 1
	ds_read_b64_tr_b16 v[52:53], v37 offset:16576
	ds_read_b64_tr_b16 v[54:55], v39 offset:16576
	ds_read_b64_tr_b16 v[118:119], v37 offset:16608
	ds_read_b64_tr_b16 v[120:121], v39 offset:16608
	s_waitcnt lgkmcnt(4)
	v_mfma_f32_16x16x32_bf16 v[60:63], v[28:31], v[20:23], v[60:63]
	s_waitcnt lgkmcnt(2)
	v_mfma_f32_16x16x32_bf16 v[74:77], v[52:55], v[20:23], v[74:77]
	s_waitcnt lgkmcnt(0)
	v_mfma_f32_16x16x32_bf16 v[20:23], v[118:121], v[20:23], v[110:113]
	s_nop 2
	ds_read_b128 v[110:113], v69 offset:1024
	s_waitcnt lgkmcnt(0)
	v_mfma_f32_16x16x32_bf16 v[82:85], v[16:19], v[110:113], v[82:85]
	v_mfma_f32_16x16x32_bf16 v[86:89], v[28:31], v[110:113], v[86:89]
	v_mfma_f32_16x16x32_bf16 v[90:93], v[52:55], v[110:113], v[90:93]
	v_mfma_f32_16x16x32_bf16 v[78:81], v[118:121], v[110:113], v[78:81]
	ds_read_b128 v[110:113], v69 offset:2048
	s_waitcnt lgkmcnt(0)
	v_mfma_f32_16x16x32_bf16 v[98:101], v[16:19], v[110:113], v[98:101]
	v_mfma_f32_16x16x32_bf16 v[102:105], v[28:31], v[110:113], v[102:105]
	v_mfma_f32_16x16x32_bf16 v[106:109], v[52:55], v[110:113], v[106:109]
	v_mfma_f32_16x16x32_bf16 v[94:97], v[118:121], v[110:113], v[94:97]
	ds_read_b128 v[110:113], v69 offset:3072
	v_mfma_f32_16x16x32_bf16 v[8:11], v[126:129], v[130:133], v[8:11]
	s_waitcnt lgkmcnt(0)
	v_mfma_f32_16x16x32_bf16 v[16:19], v[16:19], v[110:113], v[64:67]
	v_mfma_f32_16x16x32_bf16 v[64:67], v[28:31], v[110:113], v[114:117]
	ds_read_b64_tr_b16 v[28:29], v37 offset:25728
	ds_read_b64_tr_b16 v[30:31], v39 offset:25728
	v_mfma_f32_16x16x32_bf16 v[52:55], v[52:55], v[110:113], v[56:59]
	v_mfma_f32_16x16x32_bf16 v[56:59], v[118:121], v[110:113], v[8:11]
	s_nop 2
	ds_read_b128 v[8:11], v69 offset:8256
	ds_read_b64_tr_b16 v[44:45], v39 offset:25760
	s_waitcnt lgkmcnt(1)
	v_mfma_f32_16x16x32_bf16 v[110:113], v[28:31], v[8:11], v[40:43]
	s_nop 2
	ds_read_b64_tr_b16 v[42:43], v37 offset:25760
	ds_read_b64_tr_b16 v[114:115], v37 offset:25792
	ds_read_b64_tr_b16 v[116:117], v39 offset:25792
	ds_read_b64_tr_b16 v[118:119], v37 offset:25824
	ds_read_b64_tr_b16 v[120:121], v39 offset:25824
	s_waitcnt lgkmcnt(4)
	v_mfma_f32_16x16x32_bf16 v[60:63], v[42:45], v[8:11], v[60:63]
	s_waitcnt lgkmcnt(2)
	v_mfma_f32_16x16x32_bf16 v[74:77], v[114:117], v[8:11], v[74:77]
	s_waitcnt lgkmcnt(0)
	v_mfma_f32_16x16x32_bf16 v[122:125], v[118:121], v[8:11], v[20:23]
	ds_read_b128 v[8:11], v69 offset:9280
	s_nop 1
	v_add_u32_e32 v20, 0xc000, v36
	v_mov_b32_e32 v21, v3
	v_lshl_add_u64 v[40:41], v[20:21], 1, s[28:29]
	v_add_co_u32_e64 v20, s[46:47], s65, v40
	s_waitcnt lgkmcnt(0)
	v_mfma_f32_16x16x32_bf16 v[82:85], v[28:31], v[8:11], v[82:85]
	v_addc_co_u32_e64 v21, s[46:47], 0, v41, s[46:47]
	global_load_dwordx4 v[126:129], v[40:41], off
	global_load_dwordx4 v[130:133], v[20:21], off
	v_mfma_f32_16x16x32_bf16 v[86:89], v[42:45], v[8:11], v[86:89]
	ds_read_b128 v[20:23], v69 offset:10304
	v_mfma_f32_16x16x32_bf16 v[90:93], v[114:117], v[8:11], v[90:93]
	v_mfma_f32_16x16x32_bf16 v[78:81], v[118:121], v[8:11], v[78:81]
	v_add_co_u32_e64 v8, s[46:47], s69, v40
	s_nop 1
	v_addc_co_u32_e64 v9, s[46:47], 0, v41, s[46:47]
	v_add_co_u32_e64 v10, s[46:47], s90, v40
	s_waitcnt lgkmcnt(0)
	v_mfma_f32_16x16x32_bf16 v[98:101], v[28:31], v[20:23], v[98:101]
	v_addc_co_u32_e64 v11, s[46:47], 0, v41, s[46:47]
	global_load_dwordx4 v[134:137], v[8:9], off
	global_load_dwordx4 v[138:141], v[10:11], off
	ds_read_b128 v[158:161], v69 offset:11328
	v_add_u32_e32 v8, 0x100, v38
	v_mov_b32_e32 v9, v3
	v_add_u32_e32 v10, 0x6100, v50
	v_mov_b32_e32 v11, v3
	v_lshl_add_u64 v[8:9], v[8:9], 1, s[44:45]
	v_lshl_add_u64 v[10:11], v[10:11], 1, s[44:45]
	s_waitcnt lgkmcnt(0)
	v_mfma_f32_16x16x32_bf16 v[162:165], v[28:31], v[158:161], v[16:19]
	global_load_dwordx4 v[28:31], v[8:9], off
	s_nop 1
	global_load_dwordx4 v[16:19], v[10:11], off
	v_add_u32_e32 v8, 0xc100, v48
	v_mov_b32_e32 v9, v3
	v_add_u32_e32 v10, 0x12100, v49
	v_mov_b32_e32 v11, v3
	v_mfma_f32_16x16x32_bf16 v[102:105], v[42:45], v[20:23], v[102:105]
	v_lshl_add_u64 v[8:9], v[8:9], 1, s[44:45]
	v_lshl_add_u64 v[10:11], v[10:11], 1, s[44:45]
	v_mfma_f32_16x16x32_bf16 v[40:43], v[42:45], v[158:161], v[64:67]
	s_waitcnt vmcnt(9)
	s_nop 1
	v_cndmask_b32_e32 v67, v33, v35, vcc
	v_cndmask_b32_e32 v66, v32, v34, vcc
	v_cndmask_b32_e32 v65, v35, v33, vcc
	v_cndmask_b32_e32 v64, v34, v32, vcc
	s_waitcnt vmcnt(8)
	v_cndmask_b32_e32 v35, v25, v27, vcc
	v_cndmask_b32_e32 v34, v24, v26, vcc
	v_cndmask_b32_e32 v33, v27, v25, vcc
	v_cndmask_b32_e32 v32, v26, v24, vcc
	s_waitcnt vmcnt(7)
	v_cndmask_b32_e32 v27, v13, v15, vcc
	v_cndmask_b32_e32 v26, v12, v14, vcc
	v_cndmask_b32_e32 v25, v15, v13, vcc
	v_cndmask_b32_e32 v24, v14, v12, vcc
	s_waitcnt vmcnt(6)
	v_cndmask_b32_e32 v15, v5, v7, vcc
	v_cndmask_b32_e32 v14, v4, v6, vcc
	v_cndmask_b32_e32 v13, v7, v5, vcc
	v_cndmask_b32_e32 v12, v6, v4, vcc
	v_mfma_f32_16x16x32_bf16 v[106:109], v[114:117], v[20:23], v[106:109]
	v_mfma_f32_16x16x32_bf16 v[94:97], v[118:121], v[20:23], v[94:97]
	global_load_dwordx4 v[20:23], v[8:9], off
	s_nop 0
	global_load_dwordx4 v[8:11], v[10:11], off
	s_barrier
; #define LAS __attribute__((address_space(3)))
; __device__ __forceinline__ s16x4 lds_tr(lds_cptr p) { return __builtin_bit_cast(s16x4, __builtin_amdgcn_ds_read_tr16_b64_v4i16((LAS s16x4*)p)); }
;     ...
;     auto compute = [&]() __attribute__((always_inline)) {
; #pragma unroll
;         for (int kh = 0; kh < 2; ++kh) {
;             bf16x8 af[4], bfr[4];
; #pragma unroll
;             for (int m = 0; m < 4; ++m) af[m] = *(const LAS bf16x8*)(la + kh * GA_KH + m * 1024);
; #pragma unroll
;             for (int n = 0; n < 4; ++n) {
;                 const s16x4 r0 = lds_tr(lb + kh * 32 * GB_ST + n * 32), r1 = lds_tr(lb + kh * 32 * GB_ST + n * 32 + bsw);
;                 bfr[n] = (bf16x8){r0[0], r0[1], r0[2], r0[3], r1[0], r1[1], r1[2], r1[3]};
;             }
; #pragma unroll
;             for (int m = 0; m < 4; ++m)
; #pragma unroll
;                 for (int n = 0; n < 4; ++n) acc[m][n] = __builtin_amdgcn_mfma_f32_16x16x32_bf16(bfr[n], af[m], acc[m][n], 0, 0, 0);
;         }
;     };
;     ...
;             __syncthreads();
;             lstore(ra1, rb0);
;             __syncthreads();
;             if (kt + 2 < nk) gloadB(kt + 2, rb0);
;             if (kt + 3 < nk) gloadA(kt + 3, ra1);
;             compute();
	ds_write_b128 v47, v[64:67]
	ds_write_b128 v47, v[32:35] offset:2048
	ds_write_b128 v47, v[24:27] offset:4096
	ds_write_b128 v47, v[12:15] offset:6144
	s_waitcnt vmcnt(7)
	ds_write_b128 v46, v[126:129] offset:16512
	s_waitcnt vmcnt(6)
	ds_write_b128 v46, v[130:133] offset:21120
	s_waitcnt vmcnt(5)
	ds_write_b128 v46, v[134:137] offset:25728
	s_waitcnt vmcnt(4)
	ds_write_b128 v46, v[138:141] offset:30336
	s_waitcnt lgkmcnt(0)
	s_barrier
	ds_read_b64_tr_b16 v[4:5], v37 offset:16512
	ds_read_b64_tr_b16 v[6:7], v39 offset:16512
	ds_read_b128 v[24:27], v69
	ds_read_b64_tr_b16 v[34:35], v39 offset:16544
	v_mfma_f32_16x16x32_bf16 v[12:15], v[118:121], v[158:161], v[56:59]
	ds_read_b64_tr_b16 v[32:33], v37 offset:16544
	ds_read_b64_tr_b16 v[64:65], v37 offset:16576
	s_waitcnt lgkmcnt(3)
	v_mfma_f32_16x16x32_bf16 v[56:59], v[4:7], v[24:27], v[110:113]
	ds_read_b64_tr_b16 v[66:67], v39 offset:16576
	s_nop 1
	ds_read_b64_tr_b16 v[110:111], v37 offset:16608
	ds_read_b64_tr_b16 v[112:113], v39 offset:16608
	v_mfma_f32_16x16x32_bf16 v[52:55], v[114:117], v[158:161], v[52:55]
	ds_read_b128 v[114:117], v69 offset:1024
	s_waitcnt lgkmcnt(0)
	v_mfma_f32_16x16x32_bf16 v[82:85], v[4:7], v[114:117], v[82:85]
	v_mfma_f32_16x16x32_bf16 v[86:89], v[32:35], v[114:117], v[86:89]
	v_mfma_f32_16x16x32_bf16 v[90:93], v[64:67], v[114:117], v[90:93]
	v_mfma_f32_16x16x32_bf16 v[78:81], v[110:113], v[114:117], v[78:81]
	ds_read_b128 v[114:117], v69 offset:2048
	s_waitcnt lgkmcnt(0)
	v_mfma_f32_16x16x32_bf16 v[98:101], v[4:7], v[114:117], v[98:101]
	v_mfma_f32_16x16x32_bf16 v[102:105], v[32:35], v[114:117], v[102:105]
	v_mfma_f32_16x16x32_bf16 v[106:109], v[64:67], v[114:117], v[106:109]
	v_mfma_f32_16x16x32_bf16 v[94:97], v[110:113], v[114:117], v[94:97]
	ds_read_b128 v[114:117], v69 offset:3072
	v_mfma_f32_16x16x32_bf16 v[60:63], v[32:35], v[24:27], v[60:63]
	v_mfma_f32_16x16x32_bf16 v[74:77], v[64:67], v[24:27], v[74:77]
	v_mfma_f32_16x16x32_bf16 v[24:27], v[110:113], v[24:27], v[122:125]
	s_waitcnt lgkmcnt(0)
	v_mfma_f32_16x16x32_bf16 v[4:7], v[4:7], v[114:117], v[162:165]
	v_mfma_f32_16x16x32_bf16 v[40:43], v[32:35], v[114:117], v[40:43]
	ds_read_b64_tr_b16 v[32:33], v37 offset:25728
	ds_read_b64_tr_b16 v[34:35], v39 offset:25728
	v_mfma_f32_16x16x32_bf16 v[52:55], v[64:67], v[114:117], v[52:55]
	v_mfma_f32_16x16x32_bf16 v[64:67], v[110:113], v[114:117], v[12:15]
	s_nop 2
	ds_read_b128 v[12:15], v69 offset:8256
	ds_read_b64_tr_b16 v[112:113], v39 offset:25760
	ds_read_b64_tr_b16 v[110:111], v37 offset:25760
	ds_read_b64_tr_b16 v[114:115], v37 offset:25792
	ds_read_b64_tr_b16 v[116:117], v39 offset:25792
	ds_read_b64_tr_b16 v[118:119], v37 offset:25824
	ds_read_b64_tr_b16 v[120:121], v39 offset:25824
	s_waitcnt lgkmcnt(6)
	v_mfma_f32_16x16x32_bf16 v[56:59], v[32:35], v[12:15], v[56:59]
	s_waitcnt lgkmcnt(4)
	v_mfma_f32_16x16x32_bf16 v[60:63], v[110:113], v[12:15], v[60:63]
	s_waitcnt lgkmcnt(2)
	v_mfma_f32_16x16x32_bf16 v[74:77], v[114:117], v[12:15], v[74:77]
	s_waitcnt lgkmcnt(0)
	v_mfma_f32_16x16x32_bf16 v[122:125], v[118:121], v[12:15], v[24:27]
	ds_read_b128 v[12:15], v69 offset:9280
	s_nop 1
	v_add_u32_e32 v24, 0x10000, v36
	v_mov_b32_e32 v25, v3
	v_lshl_add_u64 v[44:45], v[24:25], 1, s[28:29]
	v_add_co_u32_e64 v24, s[46:47], s65, v44
	s_waitcnt lgkmcnt(0)
	v_mfma_f32_16x16x32_bf16 v[82:85], v[32:35], v[12:15], v[82:85]
	v_addc_co_u32_e64 v25, s[46:47], 0, v45, s[46:47]
	global_load_dwordx4 v[126:129], v[44:45], off
	global_load_dwordx4 v[130:133], v[24:25], off
	v_mfma_f32_16x16x32_bf16 v[86:89], v[110:113], v[12:15], v[86:89]
	ds_read_b128 v[24:27], v69 offset:10304
	v_mfma_f32_16x16x32_bf16 v[90:93], v[114:117], v[12:15], v[90:93]
	v_mfma_f32_16x16x32_bf16 v[78:81], v[118:121], v[12:15], v[78:81]
	v_add_co_u32_e64 v12, s[46:47], s69, v44
	s_nop 1
	v_addc_co_u32_e64 v13, s[46:47], 0, v45, s[46:47]
	v_add_co_u32_e64 v14, s[46:47], s90, v44
	s_waitcnt lgkmcnt(0)
	v_mfma_f32_16x16x32_bf16 v[102:105], v[110:113], v[24:27], v[102:105]
	v_addc_co_u32_e64 v15, s[46:47], 0, v45, s[46:47]
	global_load_dwordx4 v[134:137], v[12:13], off
	global_load_dwordx4 v[138:141], v[14:15], off
	ds_read_b128 v[158:161], v69 offset:11328
	v_add_u32_e32 v12, 0x140, v38
	v_mov_b32_e32 v13, v3
	v_add_u32_e32 v14, 0x6140, v50
	v_mov_b32_e32 v15, v3
	s_waitcnt lgkmcnt(0)
	v_mfma_f32_16x16x32_bf16 v[162:165], v[32:35], v[158:161], v[4:7]
	v_lshl_add_u64 v[12:13], v[12:13], 1, s[44:45]
	v_lshl_add_u64 v[14:15], v[14:15], 1, s[44:45]
	s_nop 0
	v_add_u32_e32 v4, 0xc140, v48
	v_mov_b32_e32 v5, v3
	v_add_u32_e32 v6, 0x12140, v49
	v_mov_b32_e32 v7, v3
	v_mfma_f32_16x16x32_bf16 v[40:43], v[110:113], v[158:161], v[40:43]
	v_lshl_add_u64 v[4:5], v[4:5], 1, s[44:45]
	v_lshl_add_u64 v[6:7], v[6:7], 1, s[44:45]
	s_waitcnt vmcnt(7)
	v_cndmask_b32_e32 v113, v29, v31, vcc
	v_cndmask_b32_e32 v112, v28, v30, vcc
	v_cndmask_b32_e32 v111, v31, v29, vcc
	v_cndmask_b32_e32 v110, v30, v28, vcc
	s_waitcnt vmcnt(6)
	v_cndmask_b32_e32 v31, v17, v19, vcc
	v_cndmask_b32_e32 v30, v16, v18, vcc
	v_cndmask_b32_e32 v29, v19, v17, vcc
	v_cndmask_b32_e32 v28, v18, v16, vcc
	s_waitcnt vmcnt(5)
	v_cndmask_b32_e32 v19, v21, v23, vcc
	v_cndmask_b32_e32 v18, v20, v22, vcc
	v_cndmask_b32_e32 v17, v23, v21, vcc
	v_cndmask_b32_e32 v16, v22, v20, vcc
	v_mfma_f32_16x16x32_bf16 v[98:101], v[32:35], v[24:27], v[98:101]
	global_load_dwordx4 v[32:35], v[12:13], off
	s_nop 0
	global_load_dwordx4 v[12:15], v[14:15], off
	v_mfma_f32_16x16x32_bf16 v[106:109], v[114:117], v[24:27], v[106:109]
	v_mfma_f32_16x16x32_bf16 v[94:97], v[118:121], v[24:27], v[94:97]
	global_load_dwordx4 v[24:27], v[4:5], off
	s_nop 0
	global_load_dwordx4 v[4:7], v[6:7], off
	s_barrier
;     ...
;     auto lstore = [&](const u32x4 (&ra)[4], const u32x4 (&rb)[NRB]) __attribute__((always_inline)) {
; #pragma unroll
;         for (int i = 0; i < 4; ++i) { const int row = (tid >> 3) + 32 * i, kc = tid & 7;
;             const u32x4 v = (kc & 1) ? (u32x4){ra[i][2], ra[i][3], ra[i][0], ra[i][1]} : ra[i];
;             *(u32x4*)(lds + (kc >> 2) * GA_KH + row * 64 + (kc & 3) * 16) = v; }
; #pragma unroll
;         for (int i = 0; i < 4; ++i) { const int k = bk + 16 * i;
;             u32x4 v;
;             if (B_F32) { const f32x4 x = __builtin_bit_cast(f32x4, rb[2 * i]), y = __builtin_bit_cast(f32x4, rb[2 * i + 1]);
;                 v[0] = pk2bf(x[0], x[1]); v[1] = pk2bf(x[2], x[3]); v[2] = pk2bf(y[0], y[1]); v[3] = pk2bf(y[2], y[3]); }
;             else v = rb[i];
;             *(u32x4*)(lds + GB_OFF + k * GB_ST + bnc * 16) = v; }
;     };
;     const lds_cptr la = (lds_cptr)lds + (wr * 64 + fr) * 64 + fq * 16;
;     const lds_cptr lb = (lds_cptr)lds + GB_OFF + (8 * fq + (fr >> 2) + (fq & 1) * 4) * GB_ST + wc * 128 + (fr & 3) * 8;
;     const int bsw = (fq & 1) ? -4 * GB_ST : 4 * GB_ST;
;     auto compute = [&]() __attribute__((always_inline)) {
; #pragma unroll
;         for (int kh = 0; kh < 2; ++kh) {
;             bf16x8 af[4], bfr[4];
; #pragma unroll
;             for (int m = 0; m < 4; ++m) af[m] = *(const LAS bf16x8*)(la + kh * GA_KH + m * 1024);
; #pragma unroll
;             for (int n = 0; n < 4; ++n) {
;                 const s16x4 r0 = lds_tr(lb + kh * 32 * GB_ST + n * 32), r1 = lds_tr(lb + kh * 32 * GB_ST + n * 32 + bsw);
;                 bfr[n] = (bf16x8){r0[0], r0[1], r0[2], r0[3], r1[0], r1[1], r1[2], r1[3]};
;             }
; #pragma unroll
;             for (int m = 0; m < 4; ++m)
; #pragma unroll
;                 for (int n = 0; n < 4; ++n) acc[m][n] = __builtin_amdgcn_mfma_f32_16x16x32_bf16(bfr[n], af[m], acc[m][n], 0, 0, 0);
;         }
;     };
;     ...
;     if (DEEP == 1) {
;         gloadA(0, ra0); gloadB(0, rb0); gloadA(1, ra1);
;         for (int kt = 0; kt < nk; kt += 2) {
;             __syncthreads();
;             lstore(ra0, rb0);
;             __syncthreads();
;             gloadB(kt + 1, rb0);
;             if (kt + 2 < nk) gloadA(kt + 2, ra0);
;             compute();
;             __syncthreads();
;             lstore(ra1, rb0);
;             __syncthreads();
;             if (kt + 2 < nk) gloadB(kt + 2, rb0);
	ds_write_b128 v47, v[16:19] offset:4096
	s_waitcnt vmcnt(8)
	v_cndmask_b32_e32 v19, v9, v11, vcc
	v_cndmask_b32_e32 v18, v8, v10, vcc
	v_cndmask_b32_e32 v17, v11, v9, vcc
	v_cndmask_b32_e32 v16, v10, v8, vcc
	ds_write_b128 v47, v[110:113]
	ds_write_b128 v47, v[28:31] offset:2048
	ds_write_b128 v47, v[16:19] offset:6144
	s_waitcnt vmcnt(7)
	ds_write_b128 v46, v[126:129] offset:16512
	s_waitcnt vmcnt(6)
	ds_write_b128 v46, v[130:133] offset:21120
	s_waitcnt vmcnt(5)
	ds_write_b128 v46, v[134:137] offset:25728
	s_waitcnt vmcnt(4)
	ds_write_b128 v46, v[138:141] offset:30336
	s_waitcnt lgkmcnt(0)
	s_barrier
	ds_read_b64_tr_b16 v[8:9], v37 offset:16512
	ds_read_b64_tr_b16 v[10:11], v39 offset:16512
	v_mfma_f32_16x16x32_bf16 v[16:19], v[118:121], v[158:161], v[64:67]
	ds_read_b128 v[20:23], v69
	ds_read_b64_tr_b16 v[30:31], v39 offset:16544
	ds_read_b64_tr_b16 v[28:29], v37 offset:16544
	ds_read_b64_tr_b16 v[64:65], v37 offset:16576
	ds_read_b64_tr_b16 v[66:67], v39 offset:16576
	ds_read_b64_tr_b16 v[110:111], v37 offset:16608
	ds_read_b64_tr_b16 v[112:113], v39 offset:16608
	v_mfma_f32_16x16x32_bf16 v[52:55], v[114:117], v[158:161], v[52:55]
	ds_read_b128 v[114:117], v69 offset:1024
	s_waitcnt lgkmcnt(0)
	v_mfma_f32_16x16x32_bf16 v[82:85], v[8:11], v[114:117], v[82:85]
	v_mfma_f32_16x16x32_bf16 v[86:89], v[28:31], v[114:117], v[86:89]
	v_mfma_f32_16x16x32_bf16 v[90:93], v[64:67], v[114:117], v[90:93]
	v_mfma_f32_16x16x32_bf16 v[78:81], v[110:113], v[114:117], v[78:81]
	ds_read_b128 v[114:117], v69 offset:2048
	s_waitcnt lgkmcnt(0)
	v_mfma_f32_16x16x32_bf16 v[98:101], v[8:11], v[114:117], v[98:101]
	v_mfma_f32_16x16x32_bf16 v[102:105], v[28:31], v[114:117], v[102:105]
	v_mfma_f32_16x16x32_bf16 v[106:109], v[64:67], v[114:117], v[106:109]
	v_mfma_f32_16x16x32_bf16 v[94:97], v[110:113], v[114:117], v[94:97]
	ds_read_b128 v[114:117], v69 offset:3072
	v_mfma_f32_16x16x32_bf16 v[56:59], v[8:11], v[20:23], v[56:59]
	v_mfma_f32_16x16x32_bf16 v[60:63], v[28:31], v[20:23], v[60:63]
	v_mfma_f32_16x16x32_bf16 v[74:77], v[64:67], v[20:23], v[74:77]
	v_mfma_f32_16x16x32_bf16 v[20:23], v[110:113], v[20:23], v[122:125]
	s_waitcnt lgkmcnt(0)
	v_mfma_f32_16x16x32_bf16 v[8:11], v[8:11], v[114:117], v[162:165]
	v_mfma_f32_16x16x32_bf16 v[40:43], v[28:31], v[114:117], v[40:43]
	ds_read_b64_tr_b16 v[28:29], v37 offset:25728
	ds_read_b64_tr_b16 v[30:31], v39 offset:25728
	v_mfma_f32_16x16x32_bf16 v[52:55], v[64:67], v[114:117], v[52:55]
	v_mfma_f32_16x16x32_bf16 v[64:67], v[110:113], v[114:117], v[16:19]
	s_nop 2
	ds_read_b128 v[16:19], v69 offset:8256
	ds_read_b64_tr_b16 v[112:113], v39 offset:25760
	ds_read_b64_tr_b16 v[110:111], v37 offset:25760
	ds_read_b64_tr_b16 v[114:115], v37 offset:25792
	ds_read_b64_tr_b16 v[116:117], v39 offset:25792
	ds_read_b64_tr_b16 v[118:119], v37 offset:25824
	ds_read_b64_tr_b16 v[120:121], v39 offset:25824
	s_waitcnt lgkmcnt(6)
	v_mfma_f32_16x16x32_bf16 v[56:59], v[28:31], v[16:19], v[56:59]
	s_waitcnt lgkmcnt(4)
	v_mfma_f32_16x16x32_bf16 v[60:63], v[110:113], v[16:19], v[60:63]
	s_waitcnt lgkmcnt(2)
	v_mfma_f32_16x16x32_bf16 v[74:77], v[114:117], v[16:19], v[74:77]
	s_waitcnt lgkmcnt(0)
	v_mfma_f32_16x16x32_bf16 v[122:125], v[118:121], v[16:19], v[20:23]
	ds_read_b128 v[16:19], v69 offset:9280
	s_nop 1
	v_add_u32_e32 v20, 0x14000, v36
	v_mov_b32_e32 v21, v3
	v_lshl_add_u64 v[44:45], v[20:21], 1, s[28:29]
	v_add_co_u32_e64 v20, s[46:47], s65, v44
	s_waitcnt lgkmcnt(0)
	v_mfma_f32_16x16x32_bf16 v[82:85], v[28:31], v[16:19], v[82:85]
	v_addc_co_u32_e64 v21, s[46:47], 0, v45, s[46:47]
	global_load_dwordx4 v[126:129], v[44:45], off
	global_load_dwordx4 v[130:133], v[20:21], off
	v_mfma_f32_16x16x32_bf16 v[86:89], v[110:113], v[16:19], v[86:89]
	ds_read_b128 v[20:23], v69 offset:10304
	v_mfma_f32_16x16x32_bf16 v[90:93], v[114:117], v[16:19], v[90:93]
	v_mfma_f32_16x16x32_bf16 v[78:81], v[118:121], v[16:19], v[78:81]
	v_add_co_u32_e64 v16, s[46:47], s69, v44
	s_nop 1
	v_addc_co_u32_e64 v17, s[46:47], 0, v45, s[46:47]
	v_add_co_u32_e64 v18, s[46:47], s90, v44
	s_waitcnt lgkmcnt(0)
	v_mfma_f32_16x16x32_bf16 v[102:105], v[110:113], v[20:23], v[102:105]
	v_addc_co_u32_e64 v19, s[46:47], 0, v45, s[46:47]
	global_load_dwordx4 v[134:137], v[16:17], off
	global_load_dwordx4 v[138:141], v[18:19], off
	ds_read_b128 v[158:161], v69 offset:11328
	v_add_u32_e32 v16, 0x180, v38
	v_mov_b32_e32 v17, v3
	v_add_u32_e32 v18, 0x6180, v50
	v_mov_b32_e32 v19, v3
	s_waitcnt lgkmcnt(0)
	v_mfma_f32_16x16x32_bf16 v[162:165], v[28:31], v[158:161], v[8:11]
	v_lshl_add_u64 v[16:17], v[16:17], 1, s[44:45]
	v_lshl_add_u64 v[18:19], v[18:19], 1, s[44:45]
	s_nop 0
	v_add_u32_e32 v8, 0xc180, v48
	v_mov_b32_e32 v9, v3
	v_add_u32_e32 v10, 0x12180, v49
	v_mov_b32_e32 v11, v3
	v_mfma_f32_16x16x32_bf16 v[40:43], v[110:113], v[158:161], v[40:43]
	v_lshl_add_u64 v[8:9], v[8:9], 1, s[44:45]
	v_lshl_add_u64 v[10:11], v[10:11], 1, s[44:45]
	s_waitcnt vmcnt(7)
	v_cndmask_b32_e32 v113, v33, v35, vcc
	v_cndmask_b32_e32 v112, v32, v34, vcc
	v_cndmask_b32_e32 v111, v35, v33, vcc
	v_cndmask_b32_e32 v110, v34, v32, vcc
	s_waitcnt vmcnt(6)
	v_cndmask_b32_e32 v35, v13, v15, vcc
	v_cndmask_b32_e32 v34, v12, v14, vcc
	v_cndmask_b32_e32 v33, v15, v13, vcc
	v_cndmask_b32_e32 v32, v14, v12, vcc
	s_waitcnt vmcnt(5)
	v_cndmask_b32_e32 v15, v25, v27, vcc
	v_cndmask_b32_e32 v14, v24, v26, vcc
	v_cndmask_b32_e32 v13, v27, v25, vcc
	v_cndmask_b32_e32 v12, v26, v24, vcc
	v_mfma_f32_16x16x32_bf16 v[98:101], v[28:31], v[20:23], v[98:101]
	global_load_dwordx4 v[28:31], v[16:17], off
	s_nop 0
	global_load_dwordx4 v[16:19], v[18:19], off
	v_mfma_f32_16x16x32_bf16 v[106:109], v[114:117], v[20:23], v[106:109]
	v_mfma_f32_16x16x32_bf16 v[94:97], v[118:121], v[20:23], v[94:97]
	global_load_dwordx4 v[20:23], v[8:9], off
	s_nop 0
	global_load_dwordx4 v[8:11], v[10:11], off
	s_barrier
;     ...
;     auto lstore = [&](const u32x4 (&ra)[4], const u32x4 (&rb)[NRB]) __attribute__((always_inline)) {
; #pragma unroll
;         for (int i = 0; i < 4; ++i) { const int row = (tid >> 3) + 32 * i, kc = tid & 7;
;             const u32x4 v = (kc & 1) ? (u32x4){ra[i][2], ra[i][3], ra[i][0], ra[i][1]} : ra[i];
;             *(u32x4*)(lds + (kc >> 2) * GA_KH + row * 64 + (kc & 3) * 16) = v; }
; #pragma unroll
;         for (int i = 0; i < 4; ++i) { const int k = bk + 16 * i;
;             u32x4 v;
;             if (B_F32) { const f32x4 x = __builtin_bit_cast(f32x4, rb[2 * i]), y = __builtin_bit_cast(f32x4, rb[2 * i + 1]);
;                 v[0] = pk2bf(x[0], x[1]); v[1] = pk2bf(x[2], x[3]); v[2] = pk2bf(y[0], y[1]); v[3] = pk2bf(y[2], y[3]); }
;             else v = rb[i];
;             *(u32x4*)(lds + GB_OFF + k * GB_ST + bnc * 16) = v; }
;     };
;     const lds_cptr la = (lds_cptr)lds + (wr * 64 + fr) * 64 + fq * 16;
;     const lds_cptr lb = (lds_cptr)lds + GB_OFF + (8 * fq + (fr >> 2) + (fq & 1) * 4) * GB_ST + wc * 128 + (fr & 3) * 8;
;     const int bsw = (fq & 1) ? -4 * GB_ST : 4 * GB_ST;
;     auto compute = [&]() __attribute__((always_inline)) {
; #pragma unroll
;         for (int kh = 0; kh < 2; ++kh) {
;             bf16x8 af[4], bfr[4];
; #pragma unroll
;             for (int m = 0; m < 4; ++m) af[m] = *(const LAS bf16x8*)(la + kh * GA_KH + m * 1024);
; #pragma unroll
;             for (int n = 0; n < 4; ++n) {
;                 const s16x4 r0 = lds_tr(lb + kh * 32 * GB_ST + n * 32), r1 = lds_tr(lb + kh * 32 * GB_ST + n * 32 + bsw);
;                 bfr[n] = (bf16x8){r0[0], r0[1], r0[2], r0[3], r1[0], r1[1], r1[2], r1[3]};
;             }
; #pragma unroll
;             for (int m = 0; m < 4; ++m)
; #pragma unroll
;                 for (int n = 0; n < 4; ++n) acc[m][n] = __builtin_amdgcn_mfma_f32_16x16x32_bf16(bfr[n], af[m], acc[m][n], 0, 0, 0);
;         }
;     };
;     ...
;     if (DEEP == 1) {
;         gloadA(0, ra0); gloadB(0, rb0); gloadA(1, ra1);
;         for (int kt = 0; kt < nk; kt += 2) {
;             __syncthreads();
;             lstore(ra0, rb0);
;             __syncthreads();
;             gloadB(kt + 1, rb0);
;             if (kt + 2 < nk) gloadA(kt + 2, ra0);
;             compute();
;             __syncthreads();
;             lstore(ra1, rb0);
;             __syncthreads();
;             if (kt + 2 < nk) gloadB(kt + 2, rb0);
	ds_write_b128 v47, v[12:15] offset:4096
	s_waitcnt vmcnt(8)
	v_cndmask_b32_e32 v15, v5, v7, vcc
	v_cndmask_b32_e32 v14, v4, v6, vcc
	v_cndmask_b32_e32 v13, v7, v5, vcc
	v_cndmask_b32_e32 v12, v6, v4, vcc
	ds_write_b128 v47, v[110:113]
	ds_write_b128 v47, v[32:35] offset:2048
	ds_write_b128 v47, v[12:15] offset:6144
	s_waitcnt vmcnt(7)
	ds_write_b128 v46, v[126:129] offset:16512
	s_waitcnt vmcnt(6)
	ds_write_b128 v46, v[130:133] offset:21120
	s_waitcnt vmcnt(5)
	ds_write_b128 v46, v[134:137] offset:25728
	s_waitcnt vmcnt(4)
	ds_write_b128 v46, v[138:141] offset:30336
	s_waitcnt lgkmcnt(0)
	s_barrier
	ds_read_b64_tr_b16 v[4:5], v37 offset:16512
	ds_read_b64_tr_b16 v[6:7], v39 offset:16512
	v_mfma_f32_16x16x32_bf16 v[12:15], v[118:121], v[158:161], v[64:67]
	ds_read_b128 v[24:27], v69
	ds_read_b64_tr_b16 v[34:35], v39 offset:16544
	ds_read_b64_tr_b16 v[32:33], v37 offset:16544
	ds_read_b64_tr_b16 v[64:65], v37 offset:16576
	ds_read_b64_tr_b16 v[66:67], v39 offset:16576
	ds_read_b64_tr_b16 v[110:111], v37 offset:16608
	ds_read_b64_tr_b16 v[112:113], v39 offset:16608
	v_mfma_f32_16x16x32_bf16 v[52:55], v[114:117], v[158:161], v[52:55]
	ds_read_b128 v[114:117], v69 offset:1024
	s_waitcnt lgkmcnt(0)
	v_mfma_f32_16x16x32_bf16 v[82:85], v[4:7], v[114:117], v[82:85]
	v_mfma_f32_16x16x32_bf16 v[86:89], v[32:35], v[114:117], v[86:89]
	v_mfma_f32_16x16x32_bf16 v[90:93], v[64:67], v[114:117], v[90:93]
	v_mfma_f32_16x16x32_bf16 v[78:81], v[110:113], v[114:117], v[78:81]
	ds_read_b128 v[114:117], v69 offset:2048
	s_waitcnt lgkmcnt(0)
	v_mfma_f32_16x16x32_bf16 v[98:101], v[4:7], v[114:117], v[98:101]
	v_mfma_f32_16x16x32_bf16 v[102:105], v[32:35], v[114:117], v[102:105]
	v_mfma_f32_16x16x32_bf16 v[106:109], v[64:67], v[114:117], v[106:109]
	v_mfma_f32_16x16x32_bf16 v[94:97], v[110:113], v[114:117], v[94:97]
	ds_read_b128 v[114:117], v69 offset:3072
	v_mfma_f32_16x16x32_bf16 v[56:59], v[4:7], v[24:27], v[56:59]
	v_mfma_f32_16x16x32_bf16 v[60:63], v[32:35], v[24:27], v[60:63]
	v_mfma_f32_16x16x32_bf16 v[74:77], v[64:67], v[24:27], v[74:77]
	v_mfma_f32_16x16x32_bf16 v[24:27], v[110:113], v[24:27], v[122:125]
	s_waitcnt lgkmcnt(0)
	v_mfma_f32_16x16x32_bf16 v[4:7], v[4:7], v[114:117], v[162:165]
	v_mfma_f32_16x16x32_bf16 v[32:35], v[32:35], v[114:117], v[40:43]
	v_mfma_f32_16x16x32_bf16 v[40:43], v[64:67], v[114:117], v[52:55]
	s_nop 2
	ds_read_b64_tr_b16 v[52:53], v37 offset:25728
	ds_read_b64_tr_b16 v[54:55], v39 offset:25728
	v_mfma_f32_16x16x32_bf16 v[64:67], v[110:113], v[114:117], v[12:15]
	s_nop 2
	ds_read_b128 v[12:15], v69 offset:8256
	ds_read_b64_tr_b16 v[112:113], v39 offset:25760
	ds_read_b64_tr_b16 v[110:111], v37 offset:25760
	ds_read_b64_tr_b16 v[114:115], v37 offset:25792
	ds_read_b64_tr_b16 v[116:117], v39 offset:25792
	ds_read_b64_tr_b16 v[118:119], v37 offset:25824
	ds_read_b64_tr_b16 v[120:121], v39 offset:25824
	s_waitcnt lgkmcnt(6)
	v_mfma_f32_16x16x32_bf16 v[56:59], v[52:55], v[12:15], v[56:59]
	s_waitcnt lgkmcnt(4)
	v_mfma_f32_16x16x32_bf16 v[60:63], v[110:113], v[12:15], v[60:63]
	s_waitcnt lgkmcnt(2)
	v_mfma_f32_16x16x32_bf16 v[74:77], v[114:117], v[12:15], v[74:77]
	s_waitcnt lgkmcnt(0)
	v_mfma_f32_16x16x32_bf16 v[122:125], v[118:121], v[12:15], v[24:27]
	ds_read_b128 v[12:15], v69 offset:9280
	s_nop 1
	v_add_u32_e32 v24, 0x18000, v36
	v_mov_b32_e32 v25, v3
	v_lshl_add_u64 v[44:45], v[24:25], 1, s[28:29]
	v_add_co_u32_e64 v24, s[46:47], s65, v44
	s_waitcnt lgkmcnt(0)
	v_mfma_f32_16x16x32_bf16 v[82:85], v[52:55], v[12:15], v[82:85]
	v_addc_co_u32_e64 v25, s[46:47], 0, v45, s[46:47]
	global_load_dwordx4 v[126:129], v[44:45], off
	global_load_dwordx4 v[130:133], v[24:25], off
	v_mfma_f32_16x16x32_bf16 v[86:89], v[110:113], v[12:15], v[86:89]
	ds_read_b128 v[24:27], v69 offset:10304
	v_mfma_f32_16x16x32_bf16 v[90:93], v[114:117], v[12:15], v[90:93]
	v_mfma_f32_16x16x32_bf16 v[78:81], v[118:121], v[12:15], v[78:81]
	v_add_co_u32_e64 v12, s[46:47], s69, v44
	s_nop 1
	v_addc_co_u32_e64 v13, s[46:47], 0, v45, s[46:47]
	v_add_co_u32_e64 v14, s[46:47], s90, v44
	s_waitcnt lgkmcnt(0)
	v_mfma_f32_16x16x32_bf16 v[98:101], v[52:55], v[24:27], v[98:101]
	v_addc_co_u32_e64 v15, s[46:47], 0, v45, s[46:47]
	global_load_dwordx4 v[134:137], v[12:13], off
	global_load_dwordx4 v[138:141], v[14:15], off
	ds_read_b128 v[158:161], v69 offset:11328
	v_add_u32_e32 v12, 0x1c0, v38
	v_mov_b32_e32 v13, v3
	v_add_u32_e32 v14, 0x61c0, v50
	v_mov_b32_e32 v15, v3
	s_waitcnt lgkmcnt(0)
	v_mfma_f32_16x16x32_bf16 v[50:53], v[52:55], v[158:161], v[4:7]
	v_lshl_add_u64 v[12:13], v[12:13], 1, s[44:45]
	v_lshl_add_u64 v[14:15], v[14:15], 1, s[44:45]
	global_load_dwordx4 v[162:165], v[12:13], off
	s_nop 0
	global_load_dwordx4 v[12:15], v[14:15], off
	v_add_u32_e32 v4, 0xc1c0, v48
	v_mov_b32_e32 v5, v3
	v_add_u32_e32 v6, 0x121c0, v49
	v_mov_b32_e32 v7, v3
	v_mfma_f32_16x16x32_bf16 v[102:105], v[110:113], v[24:27], v[102:105]
	v_lshl_add_u64 v[4:5], v[4:5], 1, s[44:45]
	v_lshl_add_u64 v[6:7], v[6:7], 1, s[44:45]
	v_add_u32_e32 v44, 0x1c000, v36
	v_mfma_f32_16x16x32_bf16 v[32:35], v[110:113], v[158:161], v[32:35]
	s_waitcnt vmcnt(9)
	v_cndmask_b32_e32 v113, v29, v31, vcc
	v_cndmask_b32_e32 v112, v28, v30, vcc
	v_cndmask_b32_e32 v111, v31, v29, vcc
	v_cndmask_b32_e32 v110, v30, v28, vcc
	s_waitcnt vmcnt(8)
	v_cndmask_b32_e32 v31, v17, v19, vcc
	v_cndmask_b32_e32 v30, v16, v18, vcc
	v_cndmask_b32_e32 v29, v19, v17, vcc
	v_cndmask_b32_e32 v28, v18, v16, vcc
	s_waitcnt vmcnt(7)
	v_cndmask_b32_e32 v19, v21, v23, vcc
	v_cndmask_b32_e32 v18, v20, v22, vcc
	v_cndmask_b32_e32 v17, v23, v21, vcc
	v_cndmask_b32_e32 v16, v22, v20, vcc
	v_mfma_f32_16x16x32_bf16 v[106:109], v[114:117], v[24:27], v[106:109]
	v_mov_b32_e32 v45, v3
	v_lshl_add_u64 v[44:45], v[44:45], 1, s[28:29]
	v_add_co_u32_e64 v70, s[46:47], s90, v44
	v_mfma_f32_16x16x32_bf16 v[94:97], v[118:121], v[24:27], v[94:97]
	global_load_dwordx4 v[24:27], v[4:5], off
	s_nop 0
	global_load_dwordx4 v[4:7], v[6:7], off
	s_barrier
;     ...
;     auto lstore = [&](const u32x4 (&ra)[4], const u32x4 (&rb)[NRB]) __attribute__((always_inline)) {
; #pragma unroll
;         for (int i = 0; i < 4; ++i) { const int row = (tid >> 3) + 32 * i, kc = tid & 7;
;             const u32x4 v = (kc & 1) ? (u32x4){ra[i][2], ra[i][3], ra[i][0], ra[i][1]} : ra[i];
;             *(u32x4*)(lds + (kc >> 2) * GA_KH + row * 64 + (kc & 3) * 16) = v; }
; #pragma unroll
;         for (int i = 0; i < 4; ++i) { const int k = bk + 16 * i;
;             u32x4 v;
;             if (B_F32) { const f32x4 x = __builtin_bit_cast(f32x4, rb[2 * i]), y = __builtin_bit_cast(f32x4, rb[2 * i + 1]);
;                 v[0] = pk2bf(x[0], x[1]); v[1] = pk2bf(x[2], x[3]); v[2] = pk2bf(y[0], y[1]); v[3] = pk2bf(y[2], y[3]); }
;             else v = rb[i];
;             *(u32x4*)(lds + GB_OFF + k * GB_ST + bnc * 16) = v; }
;     };
;     const lds_cptr la = (lds_cptr)lds + (wr * 64 + fr) * 64 + fq * 16;
;     const lds_cptr lb = (lds_cptr)lds + GB_OFF + (8 * fq + (fr >> 2) + (fq & 1) * 4) * GB_ST + wc * 128 + (fr & 3) * 8;
;     const int bsw = (fq & 1) ? -4 * GB_ST : 4 * GB_ST;
;     auto compute = [&]() __attribute__((always_inline)) {
; #pragma unroll
;         for (int kh = 0; kh < 2; ++kh) {
;             bf16x8 af[4], bfr[4];
; #pragma unroll
;             for (int m = 0; m < 4; ++m) af[m] = *(const LAS bf16x8*)(la + kh * GA_KH + m * 1024);
; #pragma unroll
;             for (int n = 0; n < 4; ++n) {
;                 const s16x4 r0 = lds_tr(lb + kh * 32 * GB_ST + n * 32), r1 = lds_tr(lb + kh * 32 * GB_ST + n * 32 + bsw);
;                 bfr[n] = (bf16x8){r0[0], r0[1], r0[2], r0[3], r1[0], r1[1], r1[2], r1[3]};
;             }
; #pragma unroll
;             for (int m = 0; m < 4; ++m)
; #pragma unroll
;                 for (int n = 0; n < 4; ++n) acc[m][n] = __builtin_amdgcn_mfma_f32_16x16x32_bf16(bfr[n], af[m], acc[m][n], 0, 0, 0);
;         }
;     };
;     ...
;     if (DEEP == 1) {
;         gloadA(0, ra0); gloadB(0, rb0); gloadA(1, ra1);
;         for (int kt = 0; kt < nk; kt += 2) {
;             __syncthreads();
;             lstore(ra0, rb0);
;             __syncthreads();
;             gloadB(kt + 1, rb0);
;             if (kt + 2 < nk) gloadA(kt + 2, ra0);
;             compute();
;             __syncthreads();
;             lstore(ra1, rb0);
;             __syncthreads();
;             if (kt + 2 < nk) gloadB(kt + 2, rb0);
	ds_write_b128 v47, v[16:19] offset:4096
	s_waitcnt vmcnt(8)
	v_cndmask_b32_e32 v19, v9, v11, vcc
	v_cndmask_b32_e32 v18, v8, v10, vcc
	v_cndmask_b32_e32 v17, v11, v9, vcc
	v_cndmask_b32_e32 v16, v10, v8, vcc
	ds_write_b128 v47, v[110:113]
	ds_write_b128 v47, v[28:31] offset:2048
	ds_write_b128 v47, v[16:19] offset:6144
	s_waitcnt vmcnt(7)
	ds_write_b128 v46, v[126:129] offset:16512
	s_waitcnt vmcnt(6)
	ds_write_b128 v46, v[130:133] offset:21120
	s_waitcnt vmcnt(5)
	ds_write_b128 v46, v[134:137] offset:25728
	s_waitcnt vmcnt(4)
	ds_write_b128 v46, v[138:141] offset:30336
	s_waitcnt lgkmcnt(0)
	s_barrier
	ds_read_b64_tr_b16 v[8:9], v37 offset:16512
	ds_read_b64_tr_b16 v[10:11], v39 offset:16512
	ds_read_b128 v[20:23], v69
	ds_read_b64_tr_b16 v[30:31], v39 offset:16544
	s_waitcnt lgkmcnt(1)
	v_mfma_f32_16x16x32_bf16 v[54:57], v[8:11], v[20:23], v[56:59]
	ds_read_b64_tr_b16 v[28:29], v37 offset:16544
	s_nop 1
	ds_read_b64_tr_b16 v[58:59], v37 offset:16576
	v_addc_co_u32_e64 v71, s[46:47], 0, v45, s[46:47]
	v_mfma_f32_16x16x32_bf16 v[16:19], v[118:121], v[158:161], v[64:67]
	s_add_u32 s28, s7, 0x1339c000
	s_addc_u32 s29, s16, 0
	s_waitcnt lgkmcnt(1)
	v_mfma_f32_16x16x32_bf16 v[62:65], v[28:31], v[20:23], v[60:63]
	s_nop 2
	ds_read_b64_tr_b16 v[60:61], v39 offset:16576
	ds_read_b64_tr_b16 v[110:111], v37 offset:16608
	ds_read_b64_tr_b16 v[112:113], v39 offset:16608
	v_mfma_f32_16x16x32_bf16 v[40:43], v[114:117], v[158:161], v[40:43]
	ds_read_b128 v[114:117], v69 offset:1024
	s_waitcnt lgkmcnt(0)
	v_mfma_f32_16x16x32_bf16 v[82:85], v[8:11], v[114:117], v[82:85]
	v_mfma_f32_16x16x32_bf16 v[86:89], v[28:31], v[114:117], v[86:89]
	v_mfma_f32_16x16x32_bf16 v[90:93], v[58:61], v[114:117], v[90:93]
	v_mfma_f32_16x16x32_bf16 v[78:81], v[110:113], v[114:117], v[78:81]
	ds_read_b128 v[114:117], v69 offset:2048
	s_waitcnt lgkmcnt(0)
	v_mfma_f32_16x16x32_bf16 v[98:101], v[8:11], v[114:117], v[98:101]
	v_mfma_f32_16x16x32_bf16 v[102:105], v[28:31], v[114:117], v[102:105]
	v_mfma_f32_16x16x32_bf16 v[106:109], v[58:61], v[114:117], v[106:109]
	v_mfma_f32_16x16x32_bf16 v[94:97], v[110:113], v[114:117], v[94:97]
	ds_read_b128 v[114:117], v69 offset:3072
	s_waitcnt lgkmcnt(0)
	v_mfma_f32_16x16x32_bf16 v[28:31], v[28:31], v[114:117], v[32:35]
	v_mfma_f32_16x16x32_bf16 v[32:35], v[58:61], v[114:117], v[40:43]
	s_nop 2
	ds_read_b64_tr_b16 v[40:41], v37 offset:25728
	ds_read_b64_tr_b16 v[42:43], v39 offset:25728
	v_mfma_f32_16x16x32_bf16 v[74:77], v[58:61], v[20:23], v[74:77]
	v_mfma_f32_16x16x32_bf16 v[8:11], v[8:11], v[114:117], v[50:53]
	s_nop 2
	ds_read_b128 v[48:51], v69 offset:8256
	ds_read_b64_tr_b16 v[58:59], v39 offset:25760
	s_waitcnt lgkmcnt(1)
	v_mfma_f32_16x16x32_bf16 v[52:55], v[40:43], v[48:51], v[54:57]
	s_nop 2
	ds_read_b64_tr_b16 v[56:57], v37 offset:25760
	ds_read_b64_tr_b16 v[60:61], v37 offset:25792
	v_mfma_f32_16x16x32_bf16 v[20:23], v[110:113], v[20:23], v[122:125]
	v_mfma_f32_16x16x32_bf16 v[16:19], v[110:113], v[114:117], v[16:19]
	s_waitcnt lgkmcnt(1)
	v_mfma_f32_16x16x32_bf16 v[64:67], v[56:59], v[48:51], v[62:65]
	s_nop 2
	ds_read_b64_tr_b16 v[62:63], v39 offset:25792
	ds_read_b64_tr_b16 v[110:111], v37 offset:25824
	ds_read_b64_tr_b16 v[112:113], v39 offset:25824
	ds_read_b128 v[114:117], v69 offset:11328
	s_waitcnt lgkmcnt(3)
	v_mfma_f32_16x16x32_bf16 v[74:77], v[60:63], v[48:51], v[74:77]
	s_waitcnt lgkmcnt(1)
	v_mfma_f32_16x16x32_bf16 v[20:23], v[110:113], v[48:51], v[20:23]
	ds_read_b128 v[48:51], v69 offset:9280
	s_waitcnt lgkmcnt(0)
	v_mfma_f32_16x16x32_bf16 v[82:85], v[40:43], v[48:51], v[82:85]
	v_mfma_f32_16x16x32_bf16 v[86:89], v[56:59], v[48:51], v[86:89]
	v_mfma_f32_16x16x32_bf16 v[90:93], v[60:63], v[48:51], v[90:93]
	v_mfma_f32_16x16x32_bf16 v[48:51], v[110:113], v[48:51], v[78:81]
	s_nop 2
	ds_read_b128 v[78:81], v69 offset:10304
	s_waitcnt lgkmcnt(0)
	v_mfma_f32_16x16x32_bf16 v[98:101], v[40:43], v[78:81], v[98:101]
	v_mfma_f32_16x16x32_bf16 v[102:105], v[56:59], v[78:81], v[102:105]
	v_mfma_f32_16x16x32_bf16 v[106:109], v[60:63], v[78:81], v[106:109]
	v_mfma_f32_16x16x32_bf16 v[78:81], v[110:113], v[78:81], v[94:97]
	s_nop 2
	v_add_co_u32_e64 v94, s[46:47], s69, v44
	v_mfma_f32_16x16x32_bf16 v[8:11], v[40:43], v[114:117], v[8:11]
	s_nop 0
	v_addc_co_u32_e64 v95, s[46:47], 0, v45, s[46:47]
	v_add_co_u32_e64 v96, s[46:47], s65, v44
	v_mfma_f32_16x16x32_bf16 v[28:31], v[56:59], v[114:117], v[28:31]
	s_nop 0
	v_addc_co_u32_e64 v97, s[46:47], 0, v45, s[46:47]
	global_load_dwordx4 v[40:43], v[44:45], off
	global_load_dwordx4 v[56:59], v[96:97], off
	s_nop 0
	global_load_dwordx4 v[94:97], v[94:95], off
	s_nop 0
	global_load_dwordx4 v[118:121], v[70:71], off
	v_mfma_f32_16x16x32_bf16 v[32:35], v[60:63], v[114:117], v[32:35]
	s_waitcnt vmcnt(7)
	v_cndmask_b32_e32 v63, v163, v165, vcc
	v_cndmask_b32_e32 v62, v162, v164, vcc
	v_cndmask_b32_e32 v61, v165, v163, vcc
	v_cndmask_b32_e32 v60, v164, v162, vcc
	s_barrier
	ds_write_b128 v47, v[60:63]
	s_waitcnt vmcnt(6)
	v_cndmask_b32_e32 v63, v13, v15, vcc
	v_cndmask_b32_e32 v62, v12, v14, vcc
	v_cndmask_b32_e32 v61, v15, v13, vcc
	v_cndmask_b32_e32 v60, v14, v12, vcc
	s_waitcnt vmcnt(5)
	v_cndmask_b32_e32 v15, v25, v27, vcc
	v_cndmask_b32_e32 v14, v24, v26, vcc
	v_cndmask_b32_e32 v13, v27, v25, vcc
	v_cndmask_b32_e32 v12, v26, v24, vcc
	ds_write_b128 v47, v[12:15] offset:4096
	s_waitcnt vmcnt(4)
	v_cndmask_b32_e32 v15, v5, v7, vcc
	v_cndmask_b32_e32 v14, v4, v6, vcc
	v_cndmask_b32_e32 v13, v7, v5, vcc
	v_cndmask_b32_e32 v12, v6, v4, vcc
	ds_write_b128 v47, v[60:63] offset:2048
	ds_write_b128 v47, v[12:15] offset:6144
	s_waitcnt vmcnt(3)
	ds_write_b128 v46, v[40:43] offset:16512
	s_waitcnt vmcnt(2)
	ds_write_b128 v46, v[56:59] offset:21120
	s_waitcnt vmcnt(1)
	ds_write_b128 v46, v[94:97] offset:25728
	s_waitcnt vmcnt(0)
	ds_write_b128 v46, v[118:121] offset:30336
	s_waitcnt lgkmcnt(0)
	s_barrier
; #define LAS __attribute__((address_space(3)))
;     template <class T> __device__ __forceinline__ T* w(size_t off) const { return (T*)(p->ws + off); }
; __device__ __forceinline__ s16x4 lds_tr(lds_cptr p) { return __builtin_bit_cast(s16x4, __builtin_amdgcn_ds_read_tr16_b64_v4i16((LAS s16x4*)p)); }
;     ...
;     auto compute = [&]() __attribute__((always_inline)) {
; #pragma unroll
;         for (int kh = 0; kh < 2; ++kh) {
;             bf16x8 af[4], bfr[4];
; #pragma unroll
;             for (int m = 0; m < 4; ++m) af[m] = *(const LAS bf16x8*)(la + kh * GA_KH + m * 1024);
; #pragma unroll
;             for (int n = 0; n < 4; ++n) {
;                 const s16x4 r0 = lds_tr(lb + kh * 32 * GB_ST + n * 32), r1 = lds_tr(lb + kh * 32 * GB_ST + n * 32 + bsw);
;                 bfr[n] = (bf16x8){r0[0], r0[1], r0[2], r0[3], r1[0], r1[1], r1[2], r1[3]};
;             }
; #pragma unroll
;             for (int m = 0; m < 4; ++m)
; #pragma unroll
;                 for (int n = 0; n < 4; ++n) acc[m][n] = __builtin_amdgcn_mfma_f32_16x16x32_bf16(bfr[n], af[m], acc[m][n], 0, 0, 0);
;         }
;     };
; __device__ __forceinline__ void s5_gemm_s(const Ctx& c, int layer, int tile, unsigned char* lds) {
;     ...
;     EPI_COORDS;
;     float* SALL = c.w<float>(WS_SALL) + (size_t)g * NCH5 * 256;
; #pragma unroll
;     for (int m = 0; m < 4; ++m)
; #pragma unroll
;         for (int n = 0; n < 4; ++n) {
;             const int row = mt * 128 + wr * 64 + m * 16 + fr, col = nt * 128 + wc * 64 + n * 16 + fq * 4;
;             if (row < NCH5) *(f32x4*)(SALL + (size_t)row * 256 + col) = acc[m][n];
;         }
	ds_read_b64_tr_b16 v[4:5], v37 offset:16512
	ds_read_b64_tr_b16 v[6:7], v39 offset:16512
	v_mfma_f32_16x16x32_bf16 v[12:15], v[110:113], v[114:117], v[16:19]
	s_nop 2
	ds_read_b128 v[16:19], v69
	ds_read_b64_tr_b16 v[26:27], v39 offset:16544
	ds_read_b64_tr_b16 v[24:25], v37 offset:16544
	ds_read_b64_tr_b16 v[44:45], v37 offset:16576
	ds_read_b64_tr_b16 v[46:47], v39 offset:16576
	ds_read_b64_tr_b16 v[56:57], v37 offset:16608
	ds_read_b64_tr_b16 v[58:59], v39 offset:16608
	s_waitcnt lgkmcnt(6)
	v_mfma_f32_16x16x32_bf16 v[40:43], v[4:7], v[16:19], v[52:55]
	v_or_b32_e32 v70, v68, v72
	v_lshrrev_b32_e32 v68, 2, v147
	v_and_b32_e32 v68, 12, v68
	s_waitcnt lgkmcnt(4)
	v_mfma_f32_16x16x32_bf16 v[52:55], v[24:27], v[16:19], v[64:67]
	s_waitcnt lgkmcnt(2)
	v_mfma_f32_16x16x32_bf16 v[60:63], v[44:47], v[16:19], v[74:77]
	s_waitcnt lgkmcnt(0)
	v_mfma_f32_16x16x32_bf16 v[16:19], v[56:59], v[16:19], v[20:23]
	s_nop 2
	ds_read_b128 v[20:23], v69 offset:1024
	s_waitcnt lgkmcnt(0)
	v_mfma_f32_16x16x32_bf16 v[74:77], v[4:7], v[20:23], v[82:85]
	v_mfma_f32_16x16x32_bf16 v[82:85], v[24:27], v[20:23], v[86:89]
	v_mfma_f32_16x16x32_bf16 v[86:89], v[44:47], v[20:23], v[90:93]
	v_mfma_f32_16x16x32_bf16 v[20:23], v[56:59], v[20:23], v[48:51]
	s_nop 2
	ds_read_b128 v[48:51], v69 offset:2048
	s_waitcnt lgkmcnt(0)
	v_mfma_f32_16x16x32_bf16 v[90:93], v[4:7], v[48:51], v[98:101]
	v_mfma_f32_16x16x32_bf16 v[94:97], v[24:27], v[48:51], v[102:105]
	v_mfma_f32_16x16x32_bf16 v[98:101], v[44:47], v[48:51], v[106:109]
	v_mfma_f32_16x16x32_bf16 v[78:81], v[56:59], v[48:51], v[78:81]
	ds_read_b128 v[48:51], v69 offset:3072
	ds_read_b64_tr_b16 v[102:103], v37 offset:25728
	ds_read_b64_tr_b16 v[104:105], v39 offset:25728
	s_waitcnt lgkmcnt(2)
	v_mfma_f32_16x16x32_bf16 v[4:7], v[4:7], v[48:51], v[8:11]
	v_mfma_f32_16x16x32_bf16 v[8:11], v[24:27], v[48:51], v[28:31]
	ds_read_b128 v[24:27], v69 offset:8256
	ds_read_b64_tr_b16 v[112:113], v39 offset:25760
	ds_read_b64_tr_b16 v[110:111], v37 offset:25760
	ds_read_b64_tr_b16 v[114:115], v37 offset:25792
	ds_read_b64_tr_b16 v[116:117], v39 offset:25792
	ds_read_b64_tr_b16 v[36:37], v37 offset:25824
	ds_read_b64_tr_b16 v[38:39], v39 offset:25824
	v_mfma_f32_16x16x32_bf16 v[28:31], v[44:47], v[48:51], v[32:35]
	s_nop 2
	ds_read_b128 v[32:35], v69 offset:10304
	s_waitcnt lgkmcnt(1)
	v_mfma_f32_16x16x32_bf16 v[64:67], v[36:39], v[24:27], v[16:19]
	s_nop 2
	ds_read_b128 v[16:19], v69 offset:9280
	s_waitcnt lgkmcnt(0)
	v_mfma_f32_16x16x32_bf16 v[44:47], v[102:105], v[16:19], v[74:77]
	s_nop 2
	ds_read_b128 v[74:77], v69 offset:11328
	v_and_b32_e32 v69, 64, v147
	v_mfma_f32_16x16x32_bf16 v[106:109], v[56:59], v[48:51], v[12:15]
	v_or3_b32 v68, v68, v69, s6
	s_movk_i32 s6, 0x220
	v_cmp_gt_i32_e32 vcc, s6, v70
	v_mfma_f32_16x16x32_bf16 v[12:15], v[102:105], v[24:27], v[40:43]
	v_lshlrev_b32_e32 v68, 2, v68
	v_mfma_f32_16x16x32_bf16 v[40:43], v[110:113], v[24:27], v[52:55]
	v_mfma_f32_16x16x32_bf16 v[60:63], v[114:117], v[24:27], v[60:63]
	v_mfma_f32_16x16x32_bf16 v[48:51], v[110:113], v[16:19], v[82:85]
	v_mfma_f32_16x16x32_bf16 v[52:55], v[114:117], v[16:19], v[86:89]
	v_mfma_f32_16x16x32_bf16 v[56:59], v[36:39], v[16:19], v[20:23]
	v_mfma_f32_16x16x32_bf16 v[16:19], v[102:105], v[32:35], v[90:93]
	v_mfma_f32_16x16x32_bf16 v[20:23], v[110:113], v[32:35], v[94:97]
	v_mfma_f32_16x16x32_bf16 v[24:27], v[114:117], v[32:35], v[98:101]
	v_mfma_f32_16x16x32_bf16 v[32:35], v[36:39], v[32:35], v[78:81]
	s_waitcnt lgkmcnt(0)
	v_mfma_f32_16x16x32_bf16 v[4:7], v[102:105], v[74:77], v[4:7]
	v_mfma_f32_16x16x32_bf16 v[8:11], v[110:113], v[74:77], v[8:11]
	v_mfma_f32_16x16x32_bf16 v[28:31], v[114:117], v[74:77], v[28:31]
	v_mfma_f32_16x16x32_bf16 v[36:39], v[36:39], v[74:77], v[106:109]
	s_and_saveexec_b64 s[6:7], vcc
	s_cbranch_execz .LBB0_357
	v_ashrrev_i32_e32 v71, 31, v70
	v_lshlrev_b64 v[74:75], 10, v[70:71]
	v_lshl_add_u64 v[74:75], s[28:29], 0, v[74:75]
	v_mov_b32_e32 v69, v3
	v_lshl_add_u64 v[74:75], v[74:75], 0, v[68:69]
	global_store_dwordx4 v[74:75], v[12:15], off sc1
	global_store_dwordx4 v[74:75], v[40:43], off offset:64 sc1
	global_store_dwordx4 v[74:75], v[60:63], off offset:128 sc1
	global_store_dwordx4 v[74:75], v[64:67], off offset:192 sc1
.LBB0_357:
	s_or_b64 exec, exec, s[6:7]
	v_or_b32_e32 v12, 16, v70
	s_movk_i32 s6, 0x220
	v_cmp_gt_i32_e32 vcc, s6, v12
	s_and_saveexec_b64 s[6:7], vcc
	s_cbranch_execz .LBB0_359
	v_ashrrev_i32_e32 v13, 31, v12
	v_lshlrev_b64 v[12:13], 10, v[12:13]
	v_lshl_add_u64 v[12:13], s[28:29], 0, v[12:13]
	v_mov_b32_e32 v69, v3
	v_lshl_add_u64 v[12:13], v[12:13], 0, v[68:69]
	global_store_dwordx4 v[12:13], v[44:47], off sc1
	global_store_dwordx4 v[12:13], v[48:51], off offset:64 sc1
	global_store_dwordx4 v[12:13], v[52:55], off offset:128 sc1
	global_store_dwordx4 v[12:13], v[56:59], off offset:192 sc1
.LBB0_359:
	s_or_b64 exec, exec, s[6:7]
	v_or_b32_e32 v12, 32, v70
	s_movk_i32 s6, 0x220
	v_cmp_gt_i32_e32 vcc, s6, v12
	s_and_saveexec_b64 s[6:7], vcc
	s_cbranch_execz .LBB0_361
	v_ashrrev_i32_e32 v13, 31, v12
	v_lshlrev_b64 v[12:13], 10, v[12:13]
	v_lshl_add_u64 v[12:13], s[28:29], 0, v[12:13]
	v_mov_b32_e32 v69, v3
	v_lshl_add_u64 v[12:13], v[12:13], 0, v[68:69]
	global_store_dwordx4 v[12:13], v[16:19], off sc1
	global_store_dwordx4 v[12:13], v[20:23], off offset:64 sc1
	global_store_dwordx4 v[12:13], v[24:27], off offset:128 sc1
	global_store_dwordx4 v[12:13], v[32:35], off offset:192 sc1
.LBB0_361:
	s_or_b64 exec, exec, s[6:7]
	v_or_b32_e32 v12, 48, v70
	s_movk_i32 s6, 0x220
	v_cmp_gt_i32_e32 vcc, s6, v12
	s_and_saveexec_b64 s[6:7], vcc
	s_cbranch_execz .LBB0_363
	v_ashrrev_i32_e32 v13, 31, v12
	v_lshlrev_b64 v[12:13], 10, v[12:13]
	v_lshl_add_u64 v[12:13], s[28:29], 0, v[12:13]
	v_mov_b32_e32 v69, v3
	v_lshl_add_u64 v[12:13], v[12:13], 0, v[68:69]
	global_store_dwordx4 v[12:13], v[4:7], off sc1
	global_store_dwordx4 v[12:13], v[8:11], off offset:64 sc1
	global_store_dwordx4 v[12:13], v[28:31], off offset:128 sc1
	global_store_dwordx4 v[12:13], v[36:39], off offset:192 sc1

;     template <class T> __device__ __forceinline__ T* w(size_t off) const { return (T*)(p->ws + off); }
; __device__ __forceinline__ void ssd_s1(const Ctx& c, int layer, int tile, unsigned char* lds) {
;     ...
;     if (tid < 257) *(f32x4*)(c.w<float>(WS_VEC) + (size_t)((b * NCH + j) * 4 + h) * 1028 + tid * 4) = *(const f32x4*)(vec + tid * 4);
; #pragma unroll
;     for (int kk = 0; kk < 4; ++kk) {
;         if (kk + 1 < 4) { loadB(kk + 1, bfr2[(kk + 1) & 1]); asm volatile("" ::: "memory"); }
;         const bf16x8 (&bfr)[8] = bfr2[kk & 1];
;         float xv[8], xa[8], xb[8];
;         unpack8v(xraw[kk], xv);
;         const f32x4 w0 = *(const f32x4*)(vec + 512 + 32 * kk + 8 * fq), w1 = *(const f32x4*)(vec + 512 + 32 * kk + 8 * fq + 4);
;         const f32x4 r0 = *(const f32x4*)(vec + 640 + 32 * kk + 8 * fq), r1 = *(const f32x4*)(vec + 640 + 32 * kk + 8 * fq + 4);
; #pragma unroll
;         for (int i = 0; i < 4; ++i) { xa[i] = xv[i] * w0[i]; xa[4 + i] = xv[4 + i] * w1[i]; xb[i] = xv[i] * r0[i]; xb[4 + i] = xv[4 + i] * r1[i]; }
;         const bf16x8 xf = pack8(xa), xr = pack8(xb);
; #pragma unroll
;         for (int ns = 0; ns < 8; ++ns) {
;             acc[0][ns] = __builtin_amdgcn_mfma_f32_16x16x32_bf16(bfr[ns], xf, acc[0][ns], 0, 0, 0);
;             acc[1][ns] = __builtin_amdgcn_mfma_f32_16x16x32_bf16(bfr[ns], xr, acc[1][ns], 0, 0, 0);
;         }
.LBB0_373:
	s_or_b64 exec, exec, s[44:45]
	s_movk_i32 s6, 0x100
	v_cmp_lt_i32_e32 vcc, s6, v147
	s_mul_i32 s17, s28, 34
	s_waitcnt lgkmcnt(0)
	s_barrier
	s_and_saveexec_b64 s[18:19], vcc
	s_xor_b64 s[28:29], exec, s[18:19]
	s_add_i32 s6, s17, s16
	s_lshl_b32 s6, s6, 2
	s_or_b32 s6, s6, s15
	s_ashr_i32 s7, s6, 31
	s_or_saveexec_b64 s[28:29], s[28:29]
	v_mov_b64_e32 v[56:57], s[6:7]
	s_xor_b64 exec, exec, s[28:29]
	s_cbranch_execz .LBB0_377
	s_add_i32 s17, s17, s16
	s_lshl_b32 s6, s17, 2
	s_or_b32 s6, s6, s15
	v_lshlrev_b32_e32 v56, 4, v147
	s_ashr_i32 s7, s6, 31
	s_mul_i32 s16, s6, 0x1010
	ds_read_b128 v[56:59], v56
	s_mul_hi_i32 s15, s6, 0x1010
	s_add_u32 s16, s42, s16
	v_ashrrev_i32_e32 v61, 31, v60
	s_addc_u32 s17, s43, s15
	v_lshl_add_u64 v[60:61], v[60:61], 2, s[16:17]
	v_add_co_u32_e32 v60, vcc, 0x45c6000, v60
	s_nop 1
	v_addc_co_u32_e32 v61, vcc, 0, v61, vcc
	s_waitcnt lgkmcnt(0)
	global_store_dwordx4 v[60:61], v[56:59], off sc1
	s_nop 1
	v_mov_b64_e32 v[56:57], s[6:7]
.LBB0_377:
	s_or_b64 exec, exec, s[28:29]
	s_mov_b64 s[6:7], 0x1449c000
	v_lshl_add_u64 v[70:71], v[54:55], 0, s[6:7]
	s_mov_b64 s[6:7], 0x144be000
	v_lshl_add_u64 v[142:143], v[54:55], 0, s[6:7]
	s_mov_b64 s[6:7], 0x144e0000
	v_lshl_add_u64 v[186:187], v[54:55], 0, s[6:7]
	s_mov_b64 s[6:7], 0x14502000
	v_lshl_add_u64 v[188:189], v[54:55], 0, s[6:7]
	s_mov_b64 s[6:7], 0x14524000
	v_lshl_add_u64 v[190:191], v[54:55], 0, s[6:7]
	s_mov_b64 s[6:7], 0x14546000
	v_lshl_add_u64 v[192:193], v[54:55], 0, s[6:7]
	s_mov_b64 s[6:7], 0x14568000
	v_lshl_add_u64 v[194:195], v[54:55], 0, s[6:7]
	s_mov_b64 s[6:7], 0x1458a000
	v_lshl_add_u64 v[54:55], v[54:55], 0, s[6:7]
	global_load_dwordx4 v[58:61], v[70:71], off offset:64
	global_load_dwordx4 v[62:65], v[142:143], off offset:64
	global_load_dwordx4 v[66:69], v[186:187], off offset:64
	global_load_dwordx4 v[74:77], v[188:189], off offset:64
	global_load_dwordx4 v[78:81], v[190:191], off offset:64
	global_load_dwordx4 v[82:85], v[192:193], off offset:64
	global_load_dwordx4 v[86:89], v[194:195], off offset:64
	global_load_dwordx4 v[90:93], v[54:55], off offset:64
	v_lshlrev_b32_e32 v73, 2, v73
	ds_read_b128 v[94:97], v73 offset:2560
	ds_read_b128 v[98:101], v73 offset:2048
	ds_read_b128 v[102:105], v73 offset:2064
	ds_read_b128 v[106:109], v73 offset:2576
	s_waitcnt vmcnt(16)
	v_lshlrev_b32_e32 v110, 16, v36
	v_and_b32_e32 v111, 0xffff0000, v36
	v_lshlrev_b32_e32 v36, 16, v37
	v_and_b32_e32 v37, 0xffff0000, v37
	s_waitcnt lgkmcnt(3)
	v_pk_mul_f32 v[94:95], v[94:95], v[110:111]
	s_waitcnt lgkmcnt(2)
	v_pk_mul_f32 v[98:99], v[98:99], v[110:111]
	v_lshlrev_b32_e32 v110, 16, v38
	v_and_b32_e32 v111, 0xffff0000, v38
	v_pk_mul_f32 v[96:97], v[96:97], v[36:37]
	v_pk_mul_f32 v[100:101], v[100:101], v[36:37]
	v_lshlrev_b32_e32 v36, 16, v39
	v_and_b32_e32 v37, 0xffff0000, v39
	s_waitcnt lgkmcnt(0)
	v_pk_mul_f32 v[106:107], v[106:107], v[110:111]
	v_pk_mul_f32 v[102:103], v[102:103], v[110:111]
	v_pk_mul_f32 v[108:109], v[108:109], v[36:37]
	v_pk_mul_f32 v[104:105], v[104:105], v[36:37]
	v_cvt_pk_bf16_f32 v36, v98, v99
	v_cvt_pk_bf16_f32 v37, v100, v101
	v_cvt_pk_bf16_f32 v38, v102, v103
	v_cvt_pk_bf16_f32 v39, v104, v105
	v_cvt_pk_bf16_f32 v94, v94, v95
	v_cvt_pk_bf16_f32 v95, v96, v97
	v_cvt_pk_bf16_f32 v96, v106, v107
	v_cvt_pk_bf16_f32 v97, v108, v109
	s_waitcnt vmcnt(15)
	v_mfma_f32_16x16x32_bf16 v[98:101], v[16:19], v[36:39], 0
	v_lshlrev_b32_e32 v196, 16, v12
	v_and_b32_e32 v197, 0xffff0000, v12
	v_lshlrev_b32_e32 v12, 16, v13
	v_mfma_f32_16x16x32_bf16 v[16:19], v[16:19], v[94:97], 0
	v_and_b32_e32 v13, 0xffff0000, v13
	v_or_b32_e32 v52, v52, v72
	v_lshlrev_b64 v[52:53], 9, v[52:53]
	s_waitcnt vmcnt(14)
	v_mfma_f32_16x16x32_bf16 v[102:105], v[20:23], v[36:39], 0
	s_mov_b64 s[6:7], 0x14d1c000
	v_mfma_f32_16x16x32_bf16 v[20:23], v[20:23], v[94:97], 0
	s_waitcnt vmcnt(13)
	v_mfma_f32_16x16x32_bf16 v[106:109], v[24:27], v[36:39], 0
	v_mfma_f32_16x16x32_bf16 v[24:27], v[24:27], v[94:97], 0
	s_waitcnt vmcnt(12)
	v_mfma_f32_16x16x32_bf16 v[110:113], v[28:31], v[36:39], 0
	v_mfma_f32_16x16x32_bf16 v[28:31], v[28:31], v[94:97], 0
	s_waitcnt vmcnt(11)
	v_mfma_f32_16x16x32_bf16 v[114:117], v[32:35], v[36:39], 0
	v_mfma_f32_16x16x32_bf16 v[32:35], v[32:35], v[94:97], 0
	s_waitcnt vmcnt(10)
	v_mfma_f32_16x16x32_bf16 v[118:121], v[40:43], v[36:39], 0
	v_mfma_f32_16x16x32_bf16 v[40:43], v[40:43], v[94:97], 0
	s_waitcnt vmcnt(9)
	v_mfma_f32_16x16x32_bf16 v[122:125], v[44:47], v[36:39], 0
	v_mfma_f32_16x16x32_bf16 v[44:47], v[44:47], v[94:97], 0
	s_waitcnt vmcnt(8)
	v_mfma_f32_16x16x32_bf16 v[36:39], v[48:51], v[36:39], 0
	v_mfma_f32_16x16x32_bf16 v[48:51], v[48:51], v[94:97], 0
	global_load_dwordx4 v[94:97], v[70:71], off offset:128
	global_load_dwordx4 v[126:129], v[142:143], off offset:128
	global_load_dwordx4 v[130:133], v[186:187], off offset:128
	global_load_dwordx4 v[134:137], v[188:189], off offset:128
	global_load_dwordx4 v[138:141], v[190:191], off offset:128
	global_load_dwordx4 v[158:161], v[192:193], off offset:128
	global_load_dwordx4 v[162:165], v[194:195], off offset:128
	global_load_dwordx4 v[166:169], v[54:55], off offset:128
	ds_read_b128 v[170:173], v73 offset:2688
	ds_read_b128 v[174:177], v73 offset:2176
	ds_read_b128 v[178:181], v73 offset:2192
	ds_read_b128 v[182:185], v73 offset:2704
	s_waitcnt lgkmcnt(3)
	v_pk_mul_f32 v[170:171], v[170:171], v[196:197]
	s_waitcnt lgkmcnt(2)
	v_pk_mul_f32 v[174:175], v[174:175], v[196:197]
	v_lshlrev_b32_e32 v196, 16, v14
	v_and_b32_e32 v197, 0xffff0000, v14
	v_pk_mul_f32 v[172:173], v[172:173], v[12:13]
	v_pk_mul_f32 v[176:177], v[176:177], v[12:13]
	v_lshlrev_b32_e32 v12, 16, v15
	v_and_b32_e32 v13, 0xffff0000, v15
	s_waitcnt lgkmcnt(0)
; __device__ __forceinline__ void ssd_s1(const Ctx& c, int layer, int tile, unsigned char* lds) {
;     ...
; #pragma unroll
;     for (int kk = 0; kk < 4; ++kk) {
;         if (kk + 1 < 4) { loadB(kk + 1, bfr2[(kk + 1) & 1]); asm volatile("" ::: "memory"); }
;         const bf16x8 (&bfr)[8] = bfr2[kk & 1];
;         float xv[8], xa[8], xb[8];
;         unpack8v(xraw[kk], xv);
;         const f32x4 w0 = *(const f32x4*)(vec + 512 + 32 * kk + 8 * fq), w1 = *(const f32x4*)(vec + 512 + 32 * kk + 8 * fq + 4);
;         const f32x4 r0 = *(const f32x4*)(vec + 640 + 32 * kk + 8 * fq), r1 = *(const f32x4*)(vec + 640 + 32 * kk + 8 * fq + 4);
; #pragma unroll
;         for (int i = 0; i < 4; ++i) { xa[i] = xv[i] * w0[i]; xa[4 + i] = xv[4 + i] * w1[i]; xb[i] = xv[i] * r0[i]; xb[4 + i] = xv[4 + i] * r1[i]; }
;         const bf16x8 xf = pack8(xa), xr = pack8(xb);
; #pragma unroll
;         for (int ns = 0; ns < 8; ++ns) {
;             acc[0][ns] = __builtin_amdgcn_mfma_f32_16x16x32_bf16(bfr[ns], xf, acc[0][ns], 0, 0, 0);
;             acc[1][ns] = __builtin_amdgcn_mfma_f32_16x16x32_bf16(bfr[ns], xr, acc[1][ns], 0, 0, 0);
;         }
	v_pk_mul_f32 v[182:183], v[182:183], v[196:197]
	v_pk_mul_f32 v[178:179], v[178:179], v[196:197]
	v_pk_mul_f32 v[184:185], v[184:185], v[12:13]
	v_pk_mul_f32 v[180:181], v[180:181], v[12:13]
	v_cvt_pk_bf16_f32 v12, v174, v175
	v_cvt_pk_bf16_f32 v13, v176, v177
	v_cvt_pk_bf16_f32 v14, v178, v179
	v_cvt_pk_bf16_f32 v15, v180, v181
	v_cvt_pk_bf16_f32 v170, v170, v171
	v_cvt_pk_bf16_f32 v171, v172, v173
	v_cvt_pk_bf16_f32 v172, v182, v183
	v_cvt_pk_bf16_f32 v173, v184, v185
	s_waitcnt vmcnt(15)
	v_mfma_f32_16x16x32_bf16 v[98:101], v[58:61], v[12:15], v[98:101]
	v_mfma_f32_16x16x32_bf16 v[16:19], v[58:61], v[170:173], v[16:19]
	s_waitcnt vmcnt(14)
	v_mfma_f32_16x16x32_bf16 v[58:61], v[62:65], v[12:15], v[102:105]
	v_mfma_f32_16x16x32_bf16 v[20:23], v[62:65], v[170:173], v[20:23]
	s_waitcnt vmcnt(13)
	v_mfma_f32_16x16x32_bf16 v[62:65], v[66:69], v[12:15], v[106:109]
	v_mfma_f32_16x16x32_bf16 v[24:27], v[66:69], v[170:173], v[24:27]
	s_waitcnt vmcnt(12)
	v_mfma_f32_16x16x32_bf16 v[66:69], v[74:77], v[12:15], v[110:113]
	v_mfma_f32_16x16x32_bf16 v[28:31], v[74:77], v[170:173], v[28:31]
	s_waitcnt vmcnt(11)
	v_mfma_f32_16x16x32_bf16 v[74:77], v[78:81], v[12:15], v[114:117]
	v_mfma_f32_16x16x32_bf16 v[32:35], v[78:81], v[170:173], v[32:35]
	s_waitcnt vmcnt(10)
	v_mfma_f32_16x16x32_bf16 v[78:81], v[82:85], v[12:15], v[118:121]
	v_mfma_f32_16x16x32_bf16 v[40:43], v[82:85], v[170:173], v[40:43]
	s_waitcnt vmcnt(9)
	v_mfma_f32_16x16x32_bf16 v[82:85], v[86:89], v[12:15], v[122:125]
	v_mfma_f32_16x16x32_bf16 v[44:47], v[86:89], v[170:173], v[44:47]
	s_waitcnt vmcnt(8)
	v_mfma_f32_16x16x32_bf16 v[12:15], v[90:93], v[12:15], v[36:39]
	s_nop 2
	global_load_dwordx4 v[36:39], v[70:71], off offset:192
	global_load_dwordx4 v[86:89], v[142:143], off offset:192
	v_mfma_f32_16x16x32_bf16 v[48:51], v[90:93], v[170:173], v[48:51]
	global_load_dwordx4 v[90:93], v[186:187], off offset:192
	global_load_dwordx4 v[102:105], v[188:189], off offset:192
	global_load_dwordx4 v[106:109], v[190:191], off offset:192
	global_load_dwordx4 v[110:113], v[192:193], off offset:192
	global_load_dwordx4 v[114:117], v[194:195], off offset:192
	global_load_dwordx4 v[118:121], v[54:55], off offset:192
	ds_read_b128 v[122:125], v73 offset:2816
	ds_read_b128 v[170:173], v73 offset:2304
	ds_read_b128 v[174:177], v73 offset:2320
	ds_read_b128 v[178:181], v73 offset:2832
	v_lshlrev_b32_e32 v54, 16, v8
	v_and_b32_e32 v55, 0xffff0000, v8
	v_lshlrev_b32_e32 v8, 16, v9
	v_and_b32_e32 v9, 0xffff0000, v9
	s_waitcnt lgkmcnt(3)
	v_pk_mul_f32 v[70:71], v[122:123], v[54:55]
	s_waitcnt lgkmcnt(2)
	v_pk_mul_f32 v[54:55], v[170:171], v[54:55]
	v_lshlrev_b32_e32 v122, 16, v10
	v_and_b32_e32 v123, 0xffff0000, v10
	v_pk_mul_f32 v[124:125], v[124:125], v[8:9]
	v_pk_mul_f32 v[170:171], v[172:173], v[8:9]
	v_lshlrev_b32_e32 v8, 16, v11
	v_and_b32_e32 v9, 0xffff0000, v11
	s_waitcnt lgkmcnt(0)
	v_pk_mul_f32 v[142:143], v[178:179], v[122:123]
	v_pk_mul_f32 v[122:123], v[174:175], v[122:123]
	v_pk_mul_f32 v[172:173], v[180:181], v[8:9]
	v_pk_mul_f32 v[174:175], v[176:177], v[8:9]
	v_cvt_pk_bf16_f32 v8, v54, v55
	v_cvt_pk_bf16_f32 v9, v170, v171
	v_cvt_pk_bf16_f32 v10, v122, v123
	v_cvt_pk_bf16_f32 v11, v174, v175
	v_cvt_pk_bf16_f32 v122, v70, v71
	v_cvt_pk_bf16_f32 v123, v124, v125
	v_cvt_pk_bf16_f32 v124, v142, v143
	v_cvt_pk_bf16_f32 v125, v172, v173
	s_waitcnt vmcnt(15)
	v_mfma_f32_16x16x32_bf16 v[98:101], v[94:97], v[8:11], v[98:101]
	v_lshlrev_b32_e32 v54, 16, v4
	v_and_b32_e32 v55, 0xffff0000, v4
	v_lshlrev_b32_e32 v4, 16, v5
	v_mfma_f32_16x16x32_bf16 v[16:19], v[94:97], v[122:125], v[16:19]
	v_and_b32_e32 v5, 0xffff0000, v5
	s_waitcnt vmcnt(14)
	v_mfma_f32_16x16x32_bf16 v[58:61], v[126:129], v[8:11], v[58:61]
	v_mfma_f32_16x16x32_bf16 v[20:23], v[126:129], v[122:125], v[20:23]
	ds_read_b128 v[94:97], v73 offset:2960
	ds_read_b128 v[126:129], v73 offset:2944
	s_waitcnt lgkmcnt(0)
	v_pk_mul_f32 v[70:71], v[126:127], v[54:55]
	s_waitcnt vmcnt(13)
	v_mfma_f32_16x16x32_bf16 v[62:65], v[130:133], v[8:11], v[62:65]
	v_lshlrev_b32_e32 v126, 16, v6
	v_and_b32_e32 v127, 0xffff0000, v6
	v_mfma_f32_16x16x32_bf16 v[24:27], v[130:133], v[122:125], v[24:27]
	s_waitcnt vmcnt(12)
	v_mfma_f32_16x16x32_bf16 v[66:69], v[134:137], v[8:11], v[66:69]
	v_mfma_f32_16x16x32_bf16 v[28:31], v[134:137], v[122:125], v[28:31]
	ds_read_b128 v[130:133], v73 offset:2448
	ds_read_b128 v[134:137], v73 offset:2432
	s_waitcnt lgkmcnt(0)
;     template <class T> __device__ __forceinline__ T* w(size_t off) const { return (T*)(p->ws + off); }
; __device__ __forceinline__ void ssd_s1(const Ctx& c, int layer, int tile, unsigned char* lds) {
;     ...
;     for (int kk = 0; kk < 4; ++kk) {
;         if (kk + 1 < 4) { loadB(kk + 1, bfr2[(kk + 1) & 1]); asm volatile("" ::: "memory"); }
;         const bf16x8 (&bfr)[8] = bfr2[kk & 1];
;         float xv[8], xa[8], xb[8];
;         unpack8v(xraw[kk], xv);
;         const f32x4 w0 = *(const f32x4*)(vec + 512 + 32 * kk + 8 * fq), w1 = *(const f32x4*)(vec + 512 + 32 * kk + 8 * fq + 4);
;         const f32x4 r0 = *(const f32x4*)(vec + 640 + 32 * kk + 8 * fq), r1 = *(const f32x4*)(vec + 640 + 32 * kk + 8 * fq + 4);
; #pragma unroll
;         for (int i = 0; i < 4; ++i) { xa[i] = xv[i] * w0[i]; xa[4 + i] = xv[4 + i] * w1[i]; xb[i] = xv[i] * r0[i]; xb[4 + i] = xv[4 + i] * r1[i]; }
;         const bf16x8 xf = pack8(xa), xr = pack8(xb);
; #pragma unroll
;         for (int ns = 0; ns < 8; ++ns) {
;             acc[0][ns] = __builtin_amdgcn_mfma_f32_16x16x32_bf16(bfr[ns], xf, acc[0][ns], 0, 0, 0);
;             acc[1][ns] = __builtin_amdgcn_mfma_f32_16x16x32_bf16(bfr[ns], xr, acc[1][ns], 0, 0, 0);
;         }
;     }
;     const size_t sidx = (size_t)((b * NCH + j) * 4 + h) * 2;
;     float* ST = c.w<float>(WS_ST);
; #pragma unroll
;     for (int d = 0; d < 2; ++d)
; #pragma unroll
;         for (int ns = 0; ns < 8; ++ns) *(f32x4*)(ST + ((sidx + d) * 64 + wid * 16 + fr) * 128 + ns * 16 + 4 * fq) = acc[d][ns];
;     if (tid == 0) { float* TOT = c.w<float>(WS_TOT); TOT[sidx] = __expf(vec[1024]); TOT[sidx + 1] = __expf(vec[1025]); }
	v_pk_mul_f32 v[54:55], v[134:135], v[54:55]
	s_waitcnt vmcnt(11)
	v_mfma_f32_16x16x32_bf16 v[74:77], v[138:141], v[8:11], v[74:77]
	v_mul_f32_e64 v134, v94, v126
	v_mul_f32_e64 v135, v95, v127
	v_pk_mul_f32 v[94:95], v[130:131], v[126:127]
	s_waitcnt vmcnt(10)
	v_mfma_f32_16x16x32_bf16 v[78:81], v[158:161], v[8:11], v[78:81]
	v_cvt_pk_bf16_f32 v6, v94, v95
	s_waitcnt vmcnt(9)
	v_mfma_f32_16x16x32_bf16 v[82:85], v[162:165], v[8:11], v[82:85]
	s_waitcnt vmcnt(8)
	v_mfma_f32_16x16x32_bf16 v[8:11], v[166:169], v[8:11], v[12:15]
	v_mfma_f32_16x16x32_bf16 v[12:15], v[166:169], v[122:125], v[48:51]
	s_nop 2
	v_mul_f32_e64 v50, v128, v4
	v_mul_f32_e64 v51, v129, v5
	v_pk_mul_f32 v[48:49], v[136:137], v[4:5]
	v_lshlrev_b32_e32 v4, 16, v7
	v_and_b32_e32 v5, 0xffff0000, v7
	v_mfma_f32_16x16x32_bf16 v[32:35], v[138:141], v[122:125], v[32:35]
	v_mfma_f32_16x16x32_bf16 v[40:43], v[158:161], v[122:125], v[40:43]
	v_mfma_f32_16x16x32_bf16 v[44:47], v[162:165], v[122:125], v[44:47]
	v_mul_f32_e64 v122, v96, v4
	v_mul_f32_e64 v123, v97, v5
	v_pk_mul_f32 v[96:97], v[132:133], v[4:5]
	v_cvt_pk_bf16_f32 v4, v54, v55
	v_cvt_pk_bf16_f32 v5, v48, v49
	v_cvt_pk_bf16_f32 v48, v70, v71
	v_lshl_add_u64 v[54:55], s[42:43], 0, v[2:3]
	v_lshlrev_b64 v[70:71], 16, v[56:57]
	v_cvt_pk_bf16_f32 v7, v96, v97
	v_lshl_add_u64 v[54:55], v[54:55], 0, v[70:71]
	v_cvt_pk_bf16_f32 v49, v50, v51
	s_waitcnt vmcnt(7)
	v_mfma_f32_16x16x32_bf16 v[94:97], v[36:39], v[4:7], v[98:101]
	v_cvt_pk_bf16_f32 v50, v134, v135
	v_cvt_pk_bf16_f32 v51, v122, v123
	v_lshl_add_u64 v[70:71], v[54:55], 0, v[52:53]
	v_lshl_add_u64 v[72:73], v[70:71], 0, s[6:7]
	v_mfma_f32_16x16x32_bf16 v[16:19], v[36:39], v[48:51], v[16:19]
	s_mov_b32 s6, 0x14d1c000
	s_waitcnt vmcnt(6)
	v_mfma_f32_16x16x32_bf16 v[36:39], v[86:89], v[4:7], v[58:61]
	s_waitcnt vmcnt(3)
	v_mfma_f32_16x16x32_bf16 v[52:55], v[106:109], v[4:7], v[74:77]
	s_nop 2
	v_add_co_u32_e32 v74, vcc, s6, v70
	v_mfma_f32_16x16x32_bf16 v[58:61], v[90:93], v[4:7], v[62:65]
	s_nop 0
	v_addc_co_u32_e32 v75, vcc, 0, v71, vcc
	global_store_dwordx4 v[74:75], v[94:97], off sc1
	global_store_dwordx4 v[72:73], v[36:39], off offset:64 sc1
	v_mfma_f32_16x16x32_bf16 v[62:65], v[102:105], v[4:7], v[66:69]
	s_nop 2
	global_store_dwordx4 v[72:73], v[58:61], off offset:128 sc1
	s_nop 3
	global_store_dwordx4 v[72:73], v[62:65], off offset:192 sc1
	global_store_dwordx4 v[72:73], v[52:55], off offset:256 sc1
	s_waitcnt vmcnt(7)
	v_mfma_f32_16x16x32_bf16 v[66:69], v[110:113], v[4:7], v[78:81]
	s_mov_b64 s[6:7], 0x14d24000
	s_waitcnt vmcnt(6)
	v_mfma_f32_16x16x32_bf16 v[36:39], v[114:117], v[4:7], v[82:85]
	s_waitcnt vmcnt(5)
	v_mfma_f32_16x16x32_bf16 v[4:7], v[118:121], v[4:7], v[8:11]
	s_nop 2
	global_store_dwordx4 v[72:73], v[66:69], off offset:320 sc1
	s_nop 1
	global_store_dwordx4 v[72:73], v[36:39], off offset:384 sc1
	s_nop 0
	global_store_dwordx4 v[72:73], v[4:7], off offset:448 sc1
	v_mfma_f32_16x16x32_bf16 v[20:23], v[86:89], v[48:51], v[20:23]
	v_mfma_f32_16x16x32_bf16 v[24:27], v[90:93], v[48:51], v[24:27]
	v_mfma_f32_16x16x32_bf16 v[4:7], v[102:105], v[48:51], v[28:31]
	s_nop 2
	v_add_co_u32_e32 v30, vcc, 0x14d24000, v70
	v_mfma_f32_16x16x32_bf16 v[8:11], v[106:109], v[48:51], v[32:35]
	s_nop 0
	v_addc_co_u32_e32 v31, vcc, 0, v71, vcc
	v_lshl_add_u64 v[28:29], v[70:71], 0, s[6:7]
	global_store_dwordx4 v[30:31], v[16:19], off sc1
	global_store_dwordx4 v[28:29], v[20:23], off offset:64 sc1
	global_store_dwordx4 v[28:29], v[24:27], off offset:128 sc1
	global_store_dwordx4 v[28:29], v[4:7], off offset:192 sc1
	v_mfma_f32_16x16x32_bf16 v[16:19], v[110:113], v[48:51], v[40:43]
	v_cmp_eq_u32_e32 vcc, 0, v147
	v_mfma_f32_16x16x32_bf16 v[4:7], v[114:117], v[48:51], v[44:47]
	global_store_dwordx4 v[28:29], v[8:11], off offset:256 sc1
	s_nop 4
	global_store_dwordx4 v[28:29], v[16:19], off offset:320 sc1
	s_nop 0
	global_store_dwordx4 v[28:29], v[4:7], off offset:384 sc1
	s_nop 1
	v_mfma_f32_16x16x32_bf16 v[4:7], v[118:121], v[48:51], v[12:15]
	s_nop 7
	global_store_dwordx4 v[28:29], v[4:7], off offset:448 sc1
	s_and_saveexec_b64 s[6:7], vcc
	s_cbranch_execz .LBB0_352
	ds_read_b64 v[4:5], v3 offset:4096
	v_lshl_add_u64 v[6:7], v[56:57], 3, s[42:43]
	v_add_co_u32_e32 v6, vcc, 0x1801c000, v6
	s_waitcnt lgkmcnt(0)
	v_mul_f32_e32 v2, 0x3fb8aa3b, v4
	v_mul_f32_e32 v5, 0x3fb8aa3b, v5
	v_exp_f32_e32 v4, v2
	v_exp_f32_e32 v5, v5
	v_addc_co_u32_e32 v7, vcc, 0, v7, vcc
	global_store_dwordx2 v[6:7], v[4:5], off sc1
	s_branch .LBB0_352

; __device__ __forceinline__ void ph_mix1(Ctx& c, int layer, int bid, int G, unsigned char* lds, const volatile unsigned* rolew) {
;     ...
;     asm volatile("s_waitcnt vmcnt(0)" ::: "memory");
;     __syncthreads();
;     if (c.tid == 0) { __builtin_amdgcn_fence(__ATOMIC_RELEASE, "agent"); asm volatile("s_waitcnt vmcnt(0)" ::: "memory"); (void)__hip_atomic_fetch_add(l1done, 1u, __ATOMIC_RELAXED, __HIP_MEMORY_SCOPE_AGENT); }
.LBB0_381:
	s_waitcnt vmcnt(0)
	v_cmp_eq_u32_e32 vcc, 0, v147
	s_barrier
	s_and_saveexec_b64 s[6:7], vcc
	s_cbranch_execz .LBB0_384
	s_mov_b64 s[28:29], exec
	v_mbcnt_lo_u32_b32 v2, s28, 0
	s_waitcnt vmcnt(0)
	s_waitcnt vmcnt(0)
	v_mbcnt_hi_u32_b32 v2, s29, v2
	v_cmp_eq_u32_e32 vcc, 0, v2
	s_and_b64 s[16:17], exec, vcc
	s_mov_b64 exec, s[16:17]
	s_cbranch_execz .LBB0_384
	s_bcnt1_i32_b64 s15, s[28:29]
	v_mov_b32_e32 v2, s15
	global_atomic_add v3, v2, s[56:57]
